# P9 Y-slice stores as global_store instead of flat_store (no lgkmcnt coupling); plus all previous changes
# speedup vs baseline: 1.0144x; 1.0006x over previous
.LBB0_1466:
	v_add_u32_e32 v116, v171, v69
	v_add_u32_e32 v119, 0x800, v116
	ds_read2_b64 v[120:123], v119 offset0:224 offset1:240
	s_waitcnt lgkmcnt(0)
	v_pk_fma_f32 v[112:113], v[112:113], 0, v[114:115] op_sel_hi:[1,0,1]
	s_ashr_i32 s43, s42, 31
	v_pk_fma_f32 v[100:101], v[112:113], v[100:101], v[102:103]
	s_andn2_b64 vcc, exec, s[46:47]
	v_lshlrev_b32_e32 v114, 16, v122
	v_lshlrev_b32_e32 v124, 16, v123
	v_and_b32_e32 v115, 0xffff0000, v122
	v_add_f32_e32 v122, 0, v114
	v_mul_f32_e32 v114, 0x3fb8aa3b, v114
	v_exp_f32_e32 v117, v114
	v_mul_f32_e32 v114, 0x3fb8aa3b, v124
	v_exp_f32_e32 v118, v114
	v_and_b32_e32 v114, 0xffff0000, v123
	v_lshlrev_b32_e32 v123, 16, v120
	v_lshlrev_b32_e32 v125, 16, v121
	v_add_f32_e32 v128, v122, v123
	v_mul_f32_e32 v122, 0x3fb8aa3b, v123
	v_add_f32_e32 v124, 0, v124
	v_exp_f32_e32 v130, v122
	v_mul_f32_e32 v122, 0x3fb8aa3b, v125
	v_add_f32_e32 v129, v124, v125
	v_exp_f32_e32 v131, v122
	ds_read2_b64 v[122:125], v119 offset0:192 offset1:208
	v_fma_f32 v126, 0, v117, v115
	v_and_b32_e32 v120, 0xffff0000, v120
	v_fma_f32 v127, 0, v118, v114
	v_fmac_f32_e32 v120, v130, v126
	v_and_b32_e32 v121, 0xffff0000, v121
	s_waitcnt lgkmcnt(0)
	v_lshlrev_b32_e32 v126, 16, v124
	v_fmac_f32_e32 v121, v131, v127
	v_lshlrev_b32_e32 v127, 16, v125
	v_add_f32_e32 v128, v128, v126
	v_mul_f32_e32 v126, 0x3fb8aa3b, v126
	v_add_f32_e32 v129, v129, v127
	v_exp_f32_e32 v126, v126
	v_mul_f32_e32 v127, 0x3fb8aa3b, v127
	v_exp_f32_e32 v127, v127
	v_and_b32_e32 v130, 0xffff0000, v124
	v_fmac_f32_e32 v130, v126, v120
	v_and_b32_e32 v120, 0xffff0000, v125
	v_fmac_f32_e32 v120, v127, v121
	v_lshlrev_b32_e32 v121, 16, v122
	v_lshlrev_b32_e32 v124, 16, v123
	v_add_f32_e32 v128, v128, v121
	v_add_f32_e32 v129, v129, v124
	v_mul_f32_e32 v121, 0x3fb8aa3b, v121
	v_mul_f32_e32 v124, 0x3fb8aa3b, v124
	v_exp_f32_e32 v121, v121
	v_exp_f32_e32 v131, v124
	ds_read2_b64 v[124:127], v119 offset0:160 offset1:176
	v_and_b32_e32 v122, 0xffff0000, v122
	v_fmac_f32_e32 v122, v121, v130
	v_and_b32_e32 v121, 0xffff0000, v123
	v_fmac_f32_e32 v121, v131, v120
	s_waitcnt lgkmcnt(0)
	v_lshlrev_b32_e32 v120, 16, v126
	v_lshlrev_b32_e32 v123, 16, v127
	v_add_f32_e32 v128, v128, v120
	v_mul_f32_e32 v120, 0x3fb8aa3b, v120
	v_add_f32_e32 v129, v129, v123
	v_exp_f32_e32 v120, v120
	v_mul_f32_e32 v123, 0x3fb8aa3b, v123
	v_exp_f32_e32 v123, v123
	v_and_b32_e32 v126, 0xffff0000, v126
	v_fmac_f32_e32 v126, v120, v122
	v_and_b32_e32 v127, 0xffff0000, v127
	v_lshlrev_b32_e32 v120, 16, v124
	v_fmac_f32_e32 v127, v123, v121
	v_lshlrev_b32_e32 v121, 16, v125
	v_add_f32_e32 v128, v128, v120
	v_mul_f32_e32 v120, 0x3fb8aa3b, v120
	v_exp_f32_e32 v130, v120
	v_mul_f32_e32 v120, 0x3fb8aa3b, v121
	v_add_f32_e32 v129, v129, v121
	v_exp_f32_e32 v131, v120
	ds_read2_b64 v[120:123], v119 offset0:128 offset1:144
	v_and_b32_e32 v124, 0xffff0000, v124
	v_fmac_f32_e32 v124, v130, v126
	v_and_b32_e32 v125, 0xffff0000, v125
	v_fmac_f32_e32 v125, v131, v127
	s_waitcnt lgkmcnt(0)
	v_lshlrev_b32_e32 v126, 16, v122
	v_lshlrev_b32_e32 v127, 16, v123
	v_add_f32_e32 v128, v128, v126
	v_mul_f32_e32 v126, 0x3fb8aa3b, v126
	v_add_f32_e32 v129, v129, v127
	v_exp_f32_e32 v126, v126
	v_mul_f32_e32 v127, 0x3fb8aa3b, v127
	v_exp_f32_e32 v127, v127
	v_and_b32_e32 v130, 0xffff0000, v122
	v_fmac_f32_e32 v130, v126, v124
	v_and_b32_e32 v126, 0xffff0000, v123
	v_lshlrev_b32_e32 v122, 16, v120
	v_fmac_f32_e32 v126, v127, v125
	v_lshlrev_b32_e32 v123, 16, v121
	v_add_f32_e32 v127, v128, v122
	v_mul_f32_e32 v122, 0x3fb8aa3b, v122
	v_add_f32_e32 v128, v129, v123
	v_exp_f32_e32 v129, v122
	v_mul_f32_e32 v122, 0x3fb8aa3b, v123
	v_exp_f32_e32 v131, v122
	ds_read2_b64 v[122:125], v119 offset0:96 offset1:112
	v_and_b32_e32 v121, 0xffff0000, v121
	v_and_b32_e32 v120, 0xffff0000, v120
	v_fmac_f32_e32 v121, v131, v126
	v_fmac_f32_e32 v120, v129, v130
	s_waitcnt lgkmcnt(0)
	v_lshlrev_b32_e32 v126, 16, v124
	v_lshlrev_b32_e32 v129, 16, v125
	v_add_f32_e32 v127, v127, v126
	v_mul_f32_e32 v126, 0x3fb8aa3b, v126
	v_add_f32_e32 v128, v128, v129
	v_exp_f32_e32 v126, v126
	v_mul_f32_e32 v129, 0x3fb8aa3b, v129
	v_exp_f32_e32 v129, v129
	v_and_b32_e32 v130, 0xffff0000, v124
	v_fmac_f32_e32 v130, v126, v120
	v_and_b32_e32 v120, 0xffff0000, v125
	v_fmac_f32_e32 v120, v129, v121
	v_lshlrev_b32_e32 v121, 16, v122
	v_lshlrev_b32_e32 v124, 16, v123
	v_add_f32_e32 v129, v127, v121
	v_add_f32_e32 v128, v128, v124
	v_mul_f32_e32 v121, 0x3fb8aa3b, v121
	v_mul_f32_e32 v124, 0x3fb8aa3b, v124
	v_exp_f32_e32 v121, v121
	v_exp_f32_e32 v131, v124
	ds_read2_b64 v[124:127], v119 offset0:64 offset1:80
	v_and_b32_e32 v122, 0xffff0000, v122
	v_fmac_f32_e32 v122, v121, v130
	v_and_b32_e32 v121, 0xffff0000, v123
	v_fmac_f32_e32 v121, v131, v120
	s_waitcnt lgkmcnt(0)
	v_lshlrev_b32_e32 v120, 16, v126
	v_lshlrev_b32_e32 v123, 16, v127
	v_add_f32_e32 v129, v129, v120
	v_mul_f32_e32 v120, 0x3fb8aa3b, v120
	v_add_f32_e32 v128, v128, v123
	v_exp_f32_e32 v120, v120
	v_mul_f32_e32 v123, 0x3fb8aa3b, v123
	v_exp_f32_e32 v123, v123
	v_and_b32_e32 v126, 0xffff0000, v126
	v_fmac_f32_e32 v126, v120, v122
	v_and_b32_e32 v127, 0xffff0000, v127
	v_lshlrev_b32_e32 v120, 16, v124
	v_fmac_f32_e32 v127, v123, v121
	v_lshlrev_b32_e32 v121, 16, v125
	v_add_f32_e32 v129, v129, v120
	v_mul_f32_e32 v120, 0x3fb8aa3b, v120
	v_exp_f32_e32 v130, v120
	v_mul_f32_e32 v120, 0x3fb8aa3b, v121
	v_add_f32_e32 v128, v128, v121
	v_exp_f32_e32 v131, v120
	ds_read2_b64 v[120:123], v119 offset0:32 offset1:48
	v_and_b32_e32 v124, 0xffff0000, v124
	v_fmac_f32_e32 v124, v130, v126
	v_and_b32_e32 v125, 0xffff0000, v125
	v_fmac_f32_e32 v125, v131, v127
	s_waitcnt lgkmcnt(0)
	v_lshlrev_b32_e32 v126, 16, v122
	v_lshlrev_b32_e32 v127, 16, v123
	v_add_f32_e32 v129, v129, v126
	v_mul_f32_e32 v126, 0x3fb8aa3b, v126
	v_add_f32_e32 v128, v128, v127
	v_exp_f32_e32 v126, v126
	v_mul_f32_e32 v127, 0x3fb8aa3b, v127
	v_exp_f32_e32 v127, v127
	v_and_b32_e32 v130, 0xffff0000, v122
	v_fmac_f32_e32 v130, v126, v124
	v_and_b32_e32 v126, 0xffff0000, v123
	v_lshlrev_b32_e32 v122, 16, v120
	v_fmac_f32_e32 v126, v127, v125
	v_lshlrev_b32_e32 v123, 16, v121
	v_add_f32_e32 v127, v129, v122
	v_mul_f32_e32 v122, 0x3fb8aa3b, v122
	v_exp_f32_e32 v129, v122
	v_mul_f32_e32 v122, 0x3fb8aa3b, v123
	v_add_f32_e32 v128, v128, v123
	v_exp_f32_e32 v131, v122
	ds_read2_b64 v[122:125], v119 offset1:16
	v_and_b32_e32 v119, 0xffff0000, v120
	v_and_b32_e32 v120, 0xffff0000, v121
	v_fmac_f32_e32 v120, v131, v126
	v_fmac_f32_e32 v119, v129, v130
	s_waitcnt lgkmcnt(0)
	v_lshlrev_b32_e32 v121, 16, v124
	v_lshlrev_b32_e32 v126, 16, v125
	v_add_f32_e32 v127, v127, v121
	v_mul_f32_e32 v121, 0x3fb8aa3b, v121
	v_add_f32_e32 v128, v128, v126
	v_exp_f32_e32 v121, v121
	v_mul_f32_e32 v126, 0x3fb8aa3b, v126
	v_exp_f32_e32 v126, v126
	v_and_b32_e32 v129, 0xffff0000, v124
	v_fmac_f32_e32 v129, v121, v119
	v_and_b32_e32 v119, 0xffff0000, v125
	v_fmac_f32_e32 v119, v126, v120
	v_lshlrev_b32_e32 v120, 16, v122
	v_lshlrev_b32_e32 v121, 16, v123
	v_add_f32_e32 v130, v127, v120
	v_mul_f32_e32 v120, 0x3fb8aa3b, v120
	v_add_f32_e32 v128, v128, v121
	v_exp_f32_e32 v120, v120
	v_mul_f32_e32 v121, 0x3fb8aa3b, v121
	ds_read2_b64 v[124:127], v116 offset0:224 offset1:240
	v_exp_f32_e32 v121, v121
	v_and_b32_e32 v122, 0xffff0000, v122
	v_fmac_f32_e32 v122, v120, v129
	v_and_b32_e32 v120, 0xffff0000, v123
	v_fmac_f32_e32 v120, v121, v119
	s_waitcnt lgkmcnt(0)
	v_lshlrev_b32_e32 v119, 16, v126
	v_lshlrev_b32_e32 v121, 16, v127
	v_add_f32_e32 v123, v130, v119
	v_mul_f32_e32 v119, 0x3fb8aa3b, v119
	v_add_f32_e32 v128, v128, v121
	v_exp_f32_e32 v119, v119
	v_mul_f32_e32 v121, 0x3fb8aa3b, v121
	v_exp_f32_e32 v121, v121
	v_and_b32_e32 v126, 0xffff0000, v126
	v_fmac_f32_e32 v126, v119, v122
	v_and_b32_e32 v119, 0xffff0000, v127
	v_fmac_f32_e32 v119, v121, v120
	v_lshlrev_b32_e32 v120, 16, v124
	v_lshlrev_b32_e32 v121, 16, v125
	v_add_f32_e32 v127, v123, v120
	v_mul_f32_e32 v120, 0x3fb8aa3b, v120
	v_exp_f32_e32 v129, v120
	v_mul_f32_e32 v120, 0x3fb8aa3b, v121
	v_add_f32_e32 v128, v128, v121
	v_exp_f32_e32 v130, v120
	ds_read2_b64 v[120:123], v116 offset0:192 offset1:208
	v_and_b32_e32 v125, 0xffff0000, v125
	v_and_b32_e32 v124, 0xffff0000, v124
	v_fmac_f32_e32 v125, v130, v119
	v_fmac_f32_e32 v124, v129, v126
	s_waitcnt lgkmcnt(0)
	v_lshlrev_b32_e32 v119, 16, v122
	v_lshlrev_b32_e32 v126, 16, v123
	v_add_f32_e32 v127, v127, v119
	v_mul_f32_e32 v119, 0x3fb8aa3b, v119
	v_add_f32_e32 v128, v128, v126
	v_exp_f32_e32 v119, v119
	v_mul_f32_e32 v126, 0x3fb8aa3b, v126
	v_exp_f32_e32 v126, v126
	v_and_b32_e32 v129, 0xffff0000, v122
	v_fmac_f32_e32 v129, v119, v124
	v_and_b32_e32 v119, 0xffff0000, v123
	v_lshlrev_b32_e32 v122, 16, v120
	v_fmac_f32_e32 v119, v126, v125
	v_lshlrev_b32_e32 v123, 16, v121
	v_add_f32_e32 v126, v127, v122
	v_mul_f32_e32 v122, 0x3fb8aa3b, v122
	v_add_f32_e32 v127, v128, v123
	v_exp_f32_e32 v128, v122
	v_mul_f32_e32 v122, 0x3fb8aa3b, v123
	v_exp_f32_e32 v130, v122
	ds_read2_b64 v[122:125], v116 offset0:160 offset1:176
	v_and_b32_e32 v121, 0xffff0000, v121
	v_and_b32_e32 v120, 0xffff0000, v120
	v_fmac_f32_e32 v121, v130, v119
	v_fmac_f32_e32 v120, v128, v129
	s_waitcnt lgkmcnt(0)
	v_lshlrev_b32_e32 v119, 16, v124
	v_lshlrev_b32_e32 v128, 16, v125
	v_add_f32_e32 v126, v126, v119
	v_mul_f32_e32 v119, 0x3fb8aa3b, v119
	v_add_f32_e32 v127, v127, v128
	v_exp_f32_e32 v119, v119
	v_mul_f32_e32 v128, 0x3fb8aa3b, v128
	v_exp_f32_e32 v128, v128
	v_and_b32_e32 v129, 0xffff0000, v124
	v_fmac_f32_e32 v129, v119, v120
	v_and_b32_e32 v119, 0xffff0000, v125
	v_lshlrev_b32_e32 v120, 16, v122
	v_fmac_f32_e32 v119, v128, v121
	v_lshlrev_b32_e32 v121, 16, v123
	v_add_f32_e32 v128, v126, v120
	v_mul_f32_e32 v120, 0x3fb8aa3b, v120
	v_add_f32_e32 v130, v127, v121
	v_exp_f32_e32 v120, v120
	v_mul_f32_e32 v121, 0x3fb8aa3b, v121
	ds_read2_b64 v[124:127], v116 offset0:128 offset1:144
	v_exp_f32_e32 v121, v121
	v_and_b32_e32 v122, 0xffff0000, v122
	v_fmac_f32_e32 v122, v120, v129
	v_and_b32_e32 v120, 0xffff0000, v123
	v_fmac_f32_e32 v120, v121, v119
	s_waitcnt lgkmcnt(0)
	v_lshlrev_b32_e32 v119, 16, v126
	v_lshlrev_b32_e32 v121, 16, v127
	v_add_f32_e32 v123, v128, v119
	v_mul_f32_e32 v119, 0x3fb8aa3b, v119
	v_add_f32_e32 v128, v130, v121
	v_exp_f32_e32 v119, v119
	v_mul_f32_e32 v121, 0x3fb8aa3b, v121
	v_exp_f32_e32 v121, v121
	v_and_b32_e32 v126, 0xffff0000, v126
	v_fmac_f32_e32 v126, v119, v122
	v_and_b32_e32 v119, 0xffff0000, v127
	v_fmac_f32_e32 v119, v121, v120
	v_lshlrev_b32_e32 v120, 16, v124
	v_lshlrev_b32_e32 v121, 16, v125
	v_add_f32_e32 v127, v123, v120
	v_mul_f32_e32 v120, 0x3fb8aa3b, v120
	v_exp_f32_e32 v129, v120
	v_mul_f32_e32 v120, 0x3fb8aa3b, v121
	v_add_f32_e32 v128, v128, v121
	v_exp_f32_e32 v130, v120
	ds_read2_b64 v[120:123], v116 offset0:96 offset1:112
	v_and_b32_e32 v125, 0xffff0000, v125
	v_and_b32_e32 v124, 0xffff0000, v124
	v_fmac_f32_e32 v125, v130, v119
	v_fmac_f32_e32 v124, v129, v126
	s_waitcnt lgkmcnt(0)
	v_lshlrev_b32_e32 v119, 16, v122
	v_lshlrev_b32_e32 v126, 16, v123
	v_add_f32_e32 v127, v127, v119
	v_mul_f32_e32 v119, 0x3fb8aa3b, v119
	v_add_f32_e32 v128, v128, v126
	v_exp_f32_e32 v119, v119
	v_mul_f32_e32 v126, 0x3fb8aa3b, v126
	v_exp_f32_e32 v126, v126
	v_and_b32_e32 v129, 0xffff0000, v122
	v_fmac_f32_e32 v129, v119, v124
	v_and_b32_e32 v119, 0xffff0000, v123
	v_lshlrev_b32_e32 v122, 16, v120
	v_fmac_f32_e32 v119, v126, v125
	v_lshlrev_b32_e32 v123, 16, v121
	v_add_f32_e32 v126, v127, v122
	v_mul_f32_e32 v122, 0x3fb8aa3b, v122
	v_add_f32_e32 v127, v128, v123
	v_exp_f32_e32 v128, v122
	v_mul_f32_e32 v122, 0x3fb8aa3b, v123
	v_exp_f32_e32 v130, v122
	ds_read2_b64 v[122:125], v116 offset0:64 offset1:80
	v_and_b32_e32 v121, 0xffff0000, v121
	v_and_b32_e32 v120, 0xffff0000, v120
	v_fmac_f32_e32 v121, v130, v119
	v_fmac_f32_e32 v120, v128, v129
	s_waitcnt lgkmcnt(0)
	v_lshlrev_b32_e32 v119, 16, v124
	v_lshlrev_b32_e32 v128, 16, v125
	v_add_f32_e32 v126, v126, v119
	v_mul_f32_e32 v119, 0x3fb8aa3b, v119
	v_add_f32_e32 v127, v127, v128
	v_exp_f32_e32 v119, v119
	v_mul_f32_e32 v128, 0x3fb8aa3b, v128
	v_exp_f32_e32 v128, v128
	v_and_b32_e32 v129, 0xffff0000, v124
	v_fmac_f32_e32 v129, v119, v120
	v_and_b32_e32 v119, 0xffff0000, v125
	v_lshlrev_b32_e32 v120, 16, v122
	v_fmac_f32_e32 v119, v128, v121
	v_lshlrev_b32_e32 v121, 16, v123
	v_add_f32_e32 v128, v126, v120
	v_mul_f32_e32 v120, 0x3fb8aa3b, v120
	v_add_f32_e32 v130, v127, v121
	v_exp_f32_e32 v120, v120
	v_mul_f32_e32 v121, 0x3fb8aa3b, v121
	ds_read2_b64 v[124:127], v116 offset0:32 offset1:48
	v_exp_f32_e32 v121, v121
	v_and_b32_e32 v122, 0xffff0000, v122
	v_fmac_f32_e32 v122, v120, v129
	v_and_b32_e32 v120, 0xffff0000, v123
	v_fmac_f32_e32 v120, v121, v119
	s_waitcnt lgkmcnt(0)
	v_lshlrev_b32_e32 v119, 16, v126
	v_lshlrev_b32_e32 v121, 16, v127
	v_add_f32_e32 v123, v128, v119
	v_mul_f32_e32 v119, 0x3fb8aa3b, v119
	v_add_f32_e32 v128, v130, v121
	v_exp_f32_e32 v119, v119
	v_mul_f32_e32 v121, 0x3fb8aa3b, v121
	v_exp_f32_e32 v121, v121
	v_and_b32_e32 v126, 0xffff0000, v126
	v_fmac_f32_e32 v126, v119, v122
	v_and_b32_e32 v119, 0xffff0000, v127
	v_fmac_f32_e32 v119, v121, v120
	v_lshlrev_b32_e32 v120, 16, v124
	v_lshlrev_b32_e32 v121, 16, v125
	v_add_f32_e32 v127, v123, v120
	v_mul_f32_e32 v120, 0x3fb8aa3b, v120
	v_exp_f32_e32 v129, v120
	v_mul_f32_e32 v120, 0x3fb8aa3b, v121
	v_add_f32_e32 v128, v128, v121
	v_exp_f32_e32 v130, v120
	ds_read2_b64 v[120:123], v116 offset1:16
	v_and_b32_e32 v125, 0xffff0000, v125
	v_and_b32_e32 v124, 0xffff0000, v124
	v_fmac_f32_e32 v125, v130, v119
	v_fmac_f32_e32 v124, v129, v126
	s_waitcnt lgkmcnt(0)
	v_lshlrev_b32_e32 v119, 16, v122
	v_lshlrev_b32_e32 v126, 16, v123
	v_add_f32_e32 v127, v127, v119
	v_mul_f32_e32 v119, 0x3fb8aa3b, v119
	v_add_f32_e32 v128, v128, v126
	v_exp_f32_e32 v119, v119
	v_mul_f32_e32 v126, 0x3fb8aa3b, v126
	v_exp_f32_e32 v126, v126
	v_and_b32_e32 v122, 0xffff0000, v122
	v_fmac_f32_e32 v122, v119, v124
	v_and_b32_e32 v119, 0xffff0000, v123
	v_lshlrev_b32_e32 v123, 16, v120
	v_fmac_f32_e32 v119, v126, v125
	v_mul_f32_e32 v125, 0x3fb8aa3b, v123
	v_exp_f32_e32 v125, v125
	v_lshlrev_b32_e32 v124, 16, v121
	v_add_f32_e32 v123, v127, v123
	v_and_b32_e32 v120, 0xffff0000, v120
	v_fmac_f32_e32 v120, v125, v122
	v_mul_f32_e32 v122, 0x3fb8aa3b, v124
	v_mul_f32_e32 v123, 0x3fb8aa3b, v123
	v_exp_f32_e32 v122, v122
	v_exp_f32_e32 v123, v123
	v_and_b32_e32 v121, 0xffff0000, v121
	ds_bpermute_b32 v125, v168, v120
	v_fmac_f32_e32 v121, v122, v119
	ds_bpermute_b32 v119, v168, v123
	ds_bpermute_b32 v102, v167, v123
	ds_bpermute_b32 v103, v167, v120
	v_pk_fma_f32 v[100:101], v[100:101], v[104:105], v[106:107]
	ds_bpermute_b32 v107, v166, v120
	v_pk_fma_f32 v[100:101], v[100:101], v[108:109], v[110:111]
	v_add_f32_e32 v126, v128, v124
	s_waitcnt lgkmcnt(3)
	v_fmac_f32_e32 v125, v100, v119
	v_cndmask_b32_e64 v100, v125, v100, s[6:7]
	s_waitcnt lgkmcnt(1)
	v_fmac_f32_e32 v103, v100, v102
	ds_bpermute_b32 v102, v166, v123
	v_cndmask_b32_e64 v100, v100, v103, s[8:9]
	v_mul_f32_e32 v124, 0x3fb8aa3b, v126
	v_exp_f32_e32 v124, v124
	ds_bpermute_b32 v126, v168, v121
	s_waitcnt lgkmcnt(1)
	v_fmac_f32_e32 v107, v100, v102
	v_lshlrev_b32_e32 v102, 16, v236
	v_mul_f32_e32 v103, 0x3d372713, v102
	v_mul_f32_e32 v103, v103, v102
	v_fma_f32 v103, v103, v102, v102
	v_mul_f32_e32 v103, 0x3f4c422a, v103
	ds_bpermute_b32 v122, v168, v124
	v_add_f32_e32 v103, v103, v103
	v_mul_f32_e32 v103, 0x3fb8aa3b, v103
	ds_bpermute_b32 v104, v167, v124
	ds_bpermute_b32 v105, v167, v121
	v_exp_f32_e32 v103, v103
	s_waitcnt lgkmcnt(2)
	v_fmac_f32_e32 v126, v101, v122
	v_cndmask_b32_e64 v100, v100, v107, s[0:1]
	v_cndmask_b32_e64 v101, v126, v101, s[6:7]
	v_fmac_f32_e32 v115, v117, v100
	v_add_f32_e32 v100, 1.0, v103
	v_and_b32_e32 v103, 0xffff0000, v236
	s_waitcnt lgkmcnt(0)
	v_fmac_f32_e32 v105, v101, v104
	v_mul_f32_e32 v104, 0x3d372713, v103
	v_mul_f32_e32 v104, v104, v103
	v_fma_f32 v104, v104, v103, v103
	v_mul_f32_e32 v104, 0x3f4c422a, v104
	v_rcp_f32_e32 v100, v100
	v_add_f32_e32 v104, v104, v104
	v_mul_f32_e32 v104, 0x3fb8aa3b, v104
	v_exp_f32_e32 v104, v104
	ds_bpermute_b32 v106, v166, v124
	ds_bpermute_b32 v108, v166, v121
	v_fma_f32 v100, v100, -2.0, 1.0
	v_mul_f32_e32 v102, 0.5, v102
	v_add_f32_e32 v100, 1.0, v100
	v_mul_f32_e32 v100, v102, v100
	v_add_f32_e32 v102, 1.0, v104
	v_cndmask_b32_e64 v101, v101, v105, s[8:9]
	v_rcp_f32_e32 v102, v102
	s_waitcnt lgkmcnt(0)
	v_fmac_f32_e32 v108, v101, v106
	v_cndmask_b32_e64 v101, v101, v108, s[0:1]
	v_fmac_f32_e32 v114, v118, v101
	v_lshlrev_b32_e32 v101, 16, v233
	v_add_f32_e32 v101, v115, v101
	v_fma_f32 v102, v102, -2.0, 1.0
	v_mul_f32_e32 v100, v100, v101
	v_and_b32_e32 v101, 0xffff0000, v233
	v_mul_f32_e32 v103, 0.5, v103
	v_add_f32_e32 v102, 1.0, v102
	v_add_f32_e32 v101, v114, v101
	v_mul_f32_e32 v102, v103, v102
	v_mul_f32_e32 v101, v102, v101
	v_cvt_pk_bf16_f32 v102, v100, v101
	ds_read_b64 v[100:101], v116 offset:3840
	ds_write_b32 v190, v102 offset:3968
	s_add_i32 s34, s34, s35
	s_waitcnt lgkmcnt(1)
	v_lshlrev_b32_e32 v103, 16, v100
	v_mul_f32_e32 v103, 0x3fb8aa3b, v103
	v_exp_f32_e32 v103, v103
	v_and_b32_e32 v102, 0xffff0000, v100
	v_lshlrev_b32_e32 v100, 16, v101
	v_and_b32_e32 v105, 0xffff0000, v101
	v_fmac_f32_e32 v102, v115, v103
	v_lshlrev_b32_e32 v103, 16, v235
	v_mul_f32_e32 v104, 0x3d372713, v103
	v_mul_f32_e32 v104, v104, v103
	v_fma_f32 v104, v104, v103, v103
	v_mul_f32_e32 v104, 0x3f4c422a, v104
	v_add_f32_e32 v104, v104, v104
	v_mul_f32_e32 v104, 0x3fb8aa3b, v104
	v_exp_f32_e32 v104, v104
	v_mul_f32_e32 v100, 0x3fb8aa3b, v100
	v_mul_f32_e32 v103, 0.5, v103
	v_exp_f32_e32 v100, v100
	v_add_f32_e32 v101, 1.0, v104
	v_and_b32_e32 v104, 0xffff0000, v235
	v_mul_f32_e32 v106, 0x3d372713, v104
	v_mul_f32_e32 v106, v106, v104
	v_fma_f32 v106, v106, v104, v104
	v_mul_f32_e32 v106, 0x3f4c422a, v106
	v_rcp_f32_e32 v101, v101
	v_add_f32_e32 v106, v106, v106
	v_mul_f32_e32 v106, 0x3fb8aa3b, v106
	v_exp_f32_e32 v106, v106
	v_fma_f32 v101, v101, -2.0, 1.0
	v_add_f32_e32 v101, 1.0, v101
	v_mul_f32_e32 v101, v103, v101
	v_add_f32_e32 v103, 1.0, v106
	v_rcp_f32_e32 v103, v103
	v_fmac_f32_e32 v105, v114, v100
	v_lshlrev_b32_e32 v100, 16, v231
	v_add_f32_e32 v100, v102, v100
	v_fma_f32 v103, v103, -2.0, 1.0
	v_mul_f32_e32 v100, v101, v100
	v_and_b32_e32 v101, 0xffff0000, v231
	v_mul_f32_e32 v104, 0.5, v104
	v_add_f32_e32 v103, 1.0, v103
	v_add_f32_e32 v101, v105, v101
	v_mul_f32_e32 v103, v104, v103
	v_mul_f32_e32 v101, v103, v101
	v_cvt_pk_bf16_f32 v103, v100, v101
	ds_read_b64 v[100:101], v116 offset:3712
	ds_write_b32 v190, v103 offset:3840
	s_waitcnt lgkmcnt(1)
	v_lshlrev_b32_e32 v104, 16, v100
	v_mul_f32_e32 v104, 0x3fb8aa3b, v104
	v_exp_f32_e32 v104, v104
	v_and_b32_e32 v103, 0xffff0000, v100
	v_lshlrev_b32_e32 v100, 16, v101
	v_mul_f32_e32 v100, 0x3fb8aa3b, v100
	v_fmac_f32_e32 v103, v102, v104
	v_lshlrev_b32_e32 v102, 16, v234
	v_mul_f32_e32 v104, 0x3d372713, v102
	v_mul_f32_e32 v104, v104, v102
	v_fma_f32 v104, v104, v102, v102
	v_mul_f32_e32 v104, 0x3f4c422a, v104
	v_add_f32_e32 v104, v104, v104
	v_mul_f32_e32 v104, 0x3fb8aa3b, v104
	v_exp_f32_e32 v104, v104
	v_exp_f32_e32 v100, v100
	v_and_b32_e32 v106, 0xffff0000, v101
	v_mul_f32_e32 v102, 0.5, v102
	v_add_f32_e32 v101, 1.0, v104
	v_and_b32_e32 v104, 0xffff0000, v234
	v_fmac_f32_e32 v106, v105, v100
	v_mul_f32_e32 v105, 0x3d372713, v104
	v_mul_f32_e32 v105, v105, v104
	v_fma_f32 v105, v105, v104, v104
	v_mul_f32_e32 v105, 0x3f4c422a, v105
	v_rcp_f32_e32 v101, v101
	v_add_f32_e32 v105, v105, v105
	v_mul_f32_e32 v105, 0x3fb8aa3b, v105
	v_exp_f32_e32 v105, v105
	v_fma_f32 v101, v101, -2.0, 1.0
	v_add_f32_e32 v101, 1.0, v101
	v_mul_f32_e32 v101, v102, v101
	v_add_f32_e32 v102, 1.0, v105
	v_rcp_f32_e32 v102, v102
	v_lshlrev_b32_e32 v100, 16, v229
	v_add_f32_e32 v100, v103, v100
	v_mul_f32_e32 v100, v101, v100
	v_fma_f32 v102, v102, -2.0, 1.0
	v_and_b32_e32 v101, 0xffff0000, v229
	v_mul_f32_e32 v104, 0.5, v104
	v_add_f32_e32 v102, 1.0, v102
	v_add_f32_e32 v101, v106, v101
	v_mul_f32_e32 v102, v104, v102
	v_mul_f32_e32 v101, v102, v101
	v_cvt_pk_bf16_f32 v102, v100, v101
	ds_read_b64 v[100:101], v116 offset:3584
	ds_write_b32 v190, v102 offset:3712
	s_waitcnt lgkmcnt(1)
	v_lshlrev_b32_e32 v104, 16, v100
	v_mul_f32_e32 v104, 0x3fb8aa3b, v104
	v_exp_f32_e32 v104, v104
	v_and_b32_e32 v102, 0xffff0000, v100
	v_lshlrev_b32_e32 v100, 16, v101
	v_mul_f32_e32 v100, 0x3fb8aa3b, v100
	v_fmac_f32_e32 v102, v103, v104
	v_lshlrev_b32_e32 v103, 16, v232
	v_mul_f32_e32 v104, 0x3d372713, v103
	v_mul_f32_e32 v104, v104, v103
	v_fma_f32 v104, v104, v103, v103
	v_mul_f32_e32 v104, 0x3f4c422a, v104
	v_add_f32_e32 v104, v104, v104
	v_mul_f32_e32 v104, 0x3fb8aa3b, v104
	v_exp_f32_e32 v104, v104
	v_exp_f32_e32 v100, v100
	v_and_b32_e32 v105, 0xffff0000, v101
	v_mul_f32_e32 v103, 0.5, v103
	v_add_f32_e32 v101, 1.0, v104
	v_and_b32_e32 v104, 0xffff0000, v232
	v_fmac_f32_e32 v105, v106, v100
	v_mul_f32_e32 v106, 0x3d372713, v104
	v_mul_f32_e32 v106, v106, v104
	v_fma_f32 v106, v106, v104, v104
	v_mul_f32_e32 v106, 0x3f4c422a, v106
	v_rcp_f32_e32 v101, v101
	v_add_f32_e32 v106, v106, v106
	v_mul_f32_e32 v106, 0x3fb8aa3b, v106
	v_exp_f32_e32 v106, v106
	v_fma_f32 v101, v101, -2.0, 1.0
	v_add_f32_e32 v101, 1.0, v101
	v_mul_f32_e32 v101, v103, v101
	v_add_f32_e32 v103, 1.0, v106
	v_rcp_f32_e32 v103, v103
	v_lshlrev_b32_e32 v100, 16, v227
	v_add_f32_e32 v100, v102, v100
	v_mul_f32_e32 v100, v101, v100
	v_fma_f32 v103, v103, -2.0, 1.0
	v_and_b32_e32 v101, 0xffff0000, v227
	v_mul_f32_e32 v104, 0.5, v104
	v_add_f32_e32 v103, 1.0, v103
	v_add_f32_e32 v101, v105, v101
	v_mul_f32_e32 v103, v104, v103
	v_mul_f32_e32 v101, v103, v101
	v_cvt_pk_bf16_f32 v103, v100, v101
	ds_read_b64 v[100:101], v116 offset:3456
	ds_write_b32 v190, v103 offset:3584
	s_waitcnt lgkmcnt(1)
	v_lshlrev_b32_e32 v104, 16, v100
	v_mul_f32_e32 v104, 0x3fb8aa3b, v104
	v_exp_f32_e32 v104, v104
	v_and_b32_e32 v103, 0xffff0000, v100
	v_lshlrev_b32_e32 v100, 16, v101
	v_mul_f32_e32 v100, 0x3fb8aa3b, v100
	v_fmac_f32_e32 v103, v102, v104
	v_lshlrev_b32_e32 v102, 16, v230
	v_mul_f32_e32 v104, 0x3d372713, v102
	v_mul_f32_e32 v104, v104, v102
	v_fma_f32 v104, v104, v102, v102
	v_mul_f32_e32 v104, 0x3f4c422a, v104
	v_add_f32_e32 v104, v104, v104
	v_mul_f32_e32 v104, 0x3fb8aa3b, v104
	v_exp_f32_e32 v104, v104
	v_exp_f32_e32 v100, v100
	v_and_b32_e32 v106, 0xffff0000, v101
	v_mul_f32_e32 v102, 0.5, v102
	v_add_f32_e32 v101, 1.0, v104
	v_and_b32_e32 v104, 0xffff0000, v230
	v_fmac_f32_e32 v106, v105, v100
	v_mul_f32_e32 v105, 0x3d372713, v104
	v_mul_f32_e32 v105, v105, v104
	v_fma_f32 v105, v105, v104, v104
	v_mul_f32_e32 v105, 0x3f4c422a, v105
	v_rcp_f32_e32 v101, v101
	v_add_f32_e32 v105, v105, v105
	v_mul_f32_e32 v105, 0x3fb8aa3b, v105
	v_exp_f32_e32 v105, v105
	v_fma_f32 v101, v101, -2.0, 1.0
	v_add_f32_e32 v101, 1.0, v101
	v_mul_f32_e32 v101, v102, v101
	v_add_f32_e32 v102, 1.0, v105
	v_rcp_f32_e32 v102, v102
	v_lshlrev_b32_e32 v100, 16, v225
	v_add_f32_e32 v100, v103, v100
	v_mul_f32_e32 v100, v101, v100
	v_fma_f32 v102, v102, -2.0, 1.0
	v_and_b32_e32 v101, 0xffff0000, v225
	v_mul_f32_e32 v104, 0.5, v104
	v_add_f32_e32 v102, 1.0, v102
	v_add_f32_e32 v101, v106, v101
	v_mul_f32_e32 v102, v104, v102
	v_mul_f32_e32 v101, v102, v101
	v_cvt_pk_bf16_f32 v102, v100, v101
	ds_read_b64 v[100:101], v116 offset:3328
	ds_write_b32 v190, v102 offset:3456
	s_waitcnt lgkmcnt(1)
	v_lshlrev_b32_e32 v104, 16, v100
	v_mul_f32_e32 v104, 0x3fb8aa3b, v104
	v_exp_f32_e32 v104, v104
	v_and_b32_e32 v102, 0xffff0000, v100
	v_lshlrev_b32_e32 v100, 16, v101
	v_mul_f32_e32 v100, 0x3fb8aa3b, v100
	v_fmac_f32_e32 v102, v103, v104
	v_lshlrev_b32_e32 v103, 16, v228
	v_mul_f32_e32 v104, 0x3d372713, v103
	v_mul_f32_e32 v104, v104, v103
	v_fma_f32 v104, v104, v103, v103
	v_mul_f32_e32 v104, 0x3f4c422a, v104
	v_add_f32_e32 v104, v104, v104
	v_mul_f32_e32 v104, 0x3fb8aa3b, v104
	v_exp_f32_e32 v104, v104
	v_exp_f32_e32 v100, v100
	v_and_b32_e32 v105, 0xffff0000, v101
	v_mul_f32_e32 v103, 0.5, v103
	v_add_f32_e32 v101, 1.0, v104
	v_and_b32_e32 v104, 0xffff0000, v228
	v_fmac_f32_e32 v105, v106, v100
	v_mul_f32_e32 v106, 0x3d372713, v104
	v_mul_f32_e32 v106, v106, v104
	v_fma_f32 v106, v106, v104, v104
	v_mul_f32_e32 v106, 0x3f4c422a, v106
	v_rcp_f32_e32 v101, v101
	v_add_f32_e32 v106, v106, v106
	v_mul_f32_e32 v106, 0x3fb8aa3b, v106
	v_exp_f32_e32 v106, v106
	v_fma_f32 v101, v101, -2.0, 1.0
	v_add_f32_e32 v101, 1.0, v101
	v_mul_f32_e32 v101, v103, v101
	v_add_f32_e32 v103, 1.0, v106
	v_rcp_f32_e32 v103, v103
	v_lshlrev_b32_e32 v100, 16, v222
	v_add_f32_e32 v100, v102, v100
	v_mul_f32_e32 v100, v101, v100
	v_fma_f32 v103, v103, -2.0, 1.0
	v_and_b32_e32 v101, 0xffff0000, v222
	v_mul_f32_e32 v104, 0.5, v104
	v_add_f32_e32 v103, 1.0, v103
	v_add_f32_e32 v101, v105, v101
	v_mul_f32_e32 v103, v104, v103
	v_mul_f32_e32 v101, v103, v101
	v_cvt_pk_bf16_f32 v103, v100, v101
	ds_read_b64 v[100:101], v116 offset:3200
	ds_write_b32 v190, v103 offset:3328
	s_waitcnt lgkmcnt(1)
	v_lshlrev_b32_e32 v104, 16, v100
	v_mul_f32_e32 v104, 0x3fb8aa3b, v104
	v_exp_f32_e32 v104, v104
	v_and_b32_e32 v103, 0xffff0000, v100
	v_lshlrev_b32_e32 v100, 16, v101
	v_mul_f32_e32 v100, 0x3fb8aa3b, v100
	v_fmac_f32_e32 v103, v102, v104
	v_lshlrev_b32_e32 v102, 16, v226
	v_mul_f32_e32 v104, 0x3d372713, v102
	v_mul_f32_e32 v104, v104, v102
	v_fma_f32 v104, v104, v102, v102
	v_mul_f32_e32 v104, 0x3f4c422a, v104
	v_add_f32_e32 v104, v104, v104
	v_mul_f32_e32 v104, 0x3fb8aa3b, v104
	v_exp_f32_e32 v104, v104
	v_exp_f32_e32 v100, v100
	v_and_b32_e32 v106, 0xffff0000, v101
	v_mul_f32_e32 v102, 0.5, v102
	v_add_f32_e32 v101, 1.0, v104
	v_and_b32_e32 v104, 0xffff0000, v226
	v_fmac_f32_e32 v106, v105, v100
	v_mul_f32_e32 v105, 0x3d372713, v104
	v_mul_f32_e32 v105, v105, v104
	v_fma_f32 v105, v105, v104, v104
	v_mul_f32_e32 v105, 0x3f4c422a, v105
	v_rcp_f32_e32 v101, v101
	v_add_f32_e32 v105, v105, v105
	v_mul_f32_e32 v105, 0x3fb8aa3b, v105
	v_exp_f32_e32 v105, v105
	v_fma_f32 v101, v101, -2.0, 1.0
	v_add_f32_e32 v101, 1.0, v101
	v_mul_f32_e32 v101, v102, v101
	v_add_f32_e32 v102, 1.0, v105
	v_rcp_f32_e32 v102, v102
	v_lshlrev_b32_e32 v100, 16, v220
	v_add_f32_e32 v100, v103, v100
	v_mul_f32_e32 v100, v101, v100
	v_fma_f32 v102, v102, -2.0, 1.0
	v_and_b32_e32 v101, 0xffff0000, v220
	v_mul_f32_e32 v104, 0.5, v104
	v_add_f32_e32 v102, 1.0, v102
	v_add_f32_e32 v101, v106, v101
	v_mul_f32_e32 v102, v104, v102
	v_mul_f32_e32 v101, v102, v101
	v_cvt_pk_bf16_f32 v102, v100, v101
	ds_read_b64 v[100:101], v116 offset:3072
	ds_write_b32 v190, v102 offset:3200
	s_waitcnt lgkmcnt(1)
	v_lshlrev_b32_e32 v104, 16, v100
	v_mul_f32_e32 v104, 0x3fb8aa3b, v104
	v_exp_f32_e32 v104, v104
	v_and_b32_e32 v102, 0xffff0000, v100
	v_lshlrev_b32_e32 v100, 16, v101
	v_mul_f32_e32 v100, 0x3fb8aa3b, v100
	v_fmac_f32_e32 v102, v103, v104
	v_lshlrev_b32_e32 v103, 16, v224
	v_mul_f32_e32 v104, 0x3d372713, v103
	v_mul_f32_e32 v104, v104, v103
	v_fma_f32 v104, v104, v103, v103
	v_mul_f32_e32 v104, 0x3f4c422a, v104
	v_add_f32_e32 v104, v104, v104
	v_mul_f32_e32 v104, 0x3fb8aa3b, v104
	v_exp_f32_e32 v104, v104
	v_exp_f32_e32 v100, v100
	v_and_b32_e32 v105, 0xffff0000, v101
	v_mul_f32_e32 v103, 0.5, v103
	v_add_f32_e32 v101, 1.0, v104
	v_and_b32_e32 v104, 0xffff0000, v224
	v_fmac_f32_e32 v105, v106, v100
	v_mul_f32_e32 v106, 0x3d372713, v104
	v_mul_f32_e32 v106, v106, v104
	v_fma_f32 v106, v106, v104, v104
	v_mul_f32_e32 v106, 0x3f4c422a, v106
	v_rcp_f32_e32 v101, v101
	v_add_f32_e32 v106, v106, v106
	v_mul_f32_e32 v106, 0x3fb8aa3b, v106
	v_exp_f32_e32 v106, v106
	v_fma_f32 v101, v101, -2.0, 1.0
	v_add_f32_e32 v101, 1.0, v101
	v_mul_f32_e32 v101, v103, v101
	v_add_f32_e32 v103, 1.0, v106
	v_rcp_f32_e32 v103, v103
	v_lshlrev_b32_e32 v100, 16, v218
	v_add_f32_e32 v100, v102, v100
	v_mul_f32_e32 v100, v101, v100
	v_fma_f32 v103, v103, -2.0, 1.0
	v_and_b32_e32 v101, 0xffff0000, v218
	v_mul_f32_e32 v104, 0.5, v104
	v_add_f32_e32 v103, 1.0, v103
	v_add_f32_e32 v101, v105, v101
	v_mul_f32_e32 v103, v104, v103
	v_mul_f32_e32 v101, v103, v101
	v_cvt_pk_bf16_f32 v103, v100, v101
	ds_read_b64 v[100:101], v116 offset:2944
	ds_write_b32 v190, v103 offset:3072
	s_waitcnt lgkmcnt(1)
	v_lshlrev_b32_e32 v104, 16, v100
	v_mul_f32_e32 v104, 0x3fb8aa3b, v104
	v_exp_f32_e32 v104, v104
	v_and_b32_e32 v103, 0xffff0000, v100
	v_lshlrev_b32_e32 v100, 16, v101
	v_mul_f32_e32 v100, 0x3fb8aa3b, v100
	v_fmac_f32_e32 v103, v102, v104
	v_lshlrev_b32_e32 v102, 16, v223
	v_mul_f32_e32 v104, 0x3d372713, v102
	v_mul_f32_e32 v104, v104, v102
	v_fma_f32 v104, v104, v102, v102
	v_mul_f32_e32 v104, 0x3f4c422a, v104
	v_add_f32_e32 v104, v104, v104
	v_mul_f32_e32 v104, 0x3fb8aa3b, v104
	v_exp_f32_e32 v104, v104
	v_exp_f32_e32 v100, v100
	v_and_b32_e32 v106, 0xffff0000, v101
	v_mul_f32_e32 v102, 0.5, v102
	v_add_f32_e32 v101, 1.0, v104
	v_and_b32_e32 v104, 0xffff0000, v223
	v_fmac_f32_e32 v106, v105, v100
	v_mul_f32_e32 v105, 0x3d372713, v104
	v_mul_f32_e32 v105, v105, v104
	v_fma_f32 v105, v105, v104, v104
	v_mul_f32_e32 v105, 0x3f4c422a, v105
	v_rcp_f32_e32 v101, v101
	v_add_f32_e32 v105, v105, v105
	v_mul_f32_e32 v105, 0x3fb8aa3b, v105
	v_exp_f32_e32 v105, v105
	v_fma_f32 v101, v101, -2.0, 1.0
	v_add_f32_e32 v101, 1.0, v101
	v_mul_f32_e32 v101, v102, v101
	v_add_f32_e32 v102, 1.0, v105
	v_rcp_f32_e32 v102, v102
	v_lshlrev_b32_e32 v100, 16, v216
	v_add_f32_e32 v100, v103, v100
	v_mul_f32_e32 v100, v101, v100
	v_fma_f32 v102, v102, -2.0, 1.0
	v_and_b32_e32 v101, 0xffff0000, v216
	v_mul_f32_e32 v104, 0.5, v104
	v_add_f32_e32 v102, 1.0, v102
	v_add_f32_e32 v101, v106, v101
	v_mul_f32_e32 v102, v104, v102
	v_mul_f32_e32 v101, v102, v101
	v_cvt_pk_bf16_f32 v102, v100, v101
	ds_read_b64 v[100:101], v116 offset:2816
	ds_write_b32 v190, v102 offset:2944
	s_waitcnt lgkmcnt(1)
	v_lshlrev_b32_e32 v104, 16, v100
	v_mul_f32_e32 v104, 0x3fb8aa3b, v104
	v_exp_f32_e32 v104, v104
	v_and_b32_e32 v102, 0xffff0000, v100
	v_lshlrev_b32_e32 v100, 16, v101
	v_mul_f32_e32 v100, 0x3fb8aa3b, v100
	v_fmac_f32_e32 v102, v103, v104
	v_lshlrev_b32_e32 v103, 16, v221
	v_mul_f32_e32 v104, 0x3d372713, v103
	v_mul_f32_e32 v104, v104, v103
	v_fma_f32 v104, v104, v103, v103
	v_mul_f32_e32 v104, 0x3f4c422a, v104
	v_add_f32_e32 v104, v104, v104
	v_mul_f32_e32 v104, 0x3fb8aa3b, v104
	v_exp_f32_e32 v104, v104
	v_exp_f32_e32 v100, v100
	v_and_b32_e32 v105, 0xffff0000, v101
	v_mul_f32_e32 v103, 0.5, v103
	v_add_f32_e32 v101, 1.0, v104
	v_and_b32_e32 v104, 0xffff0000, v221
	v_fmac_f32_e32 v105, v106, v100
	v_mul_f32_e32 v106, 0x3d372713, v104
	v_mul_f32_e32 v106, v106, v104
	v_fma_f32 v106, v106, v104, v104
	v_mul_f32_e32 v106, 0x3f4c422a, v106
	v_rcp_f32_e32 v101, v101
	v_add_f32_e32 v106, v106, v106
	v_mul_f32_e32 v106, 0x3fb8aa3b, v106
	v_exp_f32_e32 v106, v106
	v_fma_f32 v101, v101, -2.0, 1.0
	v_add_f32_e32 v101, 1.0, v101
	v_mul_f32_e32 v101, v103, v101
	v_add_f32_e32 v103, 1.0, v106
	v_rcp_f32_e32 v103, v103
	v_lshlrev_b32_e32 v100, 16, v214
	v_add_f32_e32 v100, v102, v100
	v_mul_f32_e32 v100, v101, v100
	v_fma_f32 v103, v103, -2.0, 1.0
	v_and_b32_e32 v101, 0xffff0000, v214
	v_mul_f32_e32 v104, 0.5, v104
	v_add_f32_e32 v103, 1.0, v103
	v_add_f32_e32 v101, v105, v101
	v_mul_f32_e32 v103, v104, v103
	v_mul_f32_e32 v101, v103, v101
	v_cvt_pk_bf16_f32 v103, v100, v101
	ds_read_b64 v[100:101], v116 offset:2688
	ds_write_b32 v190, v103 offset:2816
	s_waitcnt lgkmcnt(1)
	v_lshlrev_b32_e32 v104, 16, v100
	v_mul_f32_e32 v104, 0x3fb8aa3b, v104
	v_exp_f32_e32 v104, v104
	v_and_b32_e32 v103, 0xffff0000, v100
	v_lshlrev_b32_e32 v100, 16, v101
	v_mul_f32_e32 v100, 0x3fb8aa3b, v100
	v_fmac_f32_e32 v103, v102, v104
	v_lshlrev_b32_e32 v102, 16, v219
	v_mul_f32_e32 v104, 0x3d372713, v102
	v_mul_f32_e32 v104, v104, v102
	v_fma_f32 v104, v104, v102, v102
	v_mul_f32_e32 v104, 0x3f4c422a, v104
	v_add_f32_e32 v104, v104, v104
	v_mul_f32_e32 v104, 0x3fb8aa3b, v104
	v_exp_f32_e32 v104, v104
	v_exp_f32_e32 v100, v100
	v_and_b32_e32 v106, 0xffff0000, v101
	v_mul_f32_e32 v102, 0.5, v102
	v_add_f32_e32 v101, 1.0, v104
	v_and_b32_e32 v104, 0xffff0000, v219
	v_fmac_f32_e32 v106, v105, v100
	v_mul_f32_e32 v105, 0x3d372713, v104
	v_mul_f32_e32 v105, v105, v104
	v_fma_f32 v105, v105, v104, v104
	v_mul_f32_e32 v105, 0x3f4c422a, v105
	v_rcp_f32_e32 v101, v101
	v_add_f32_e32 v105, v105, v105
	v_mul_f32_e32 v105, 0x3fb8aa3b, v105
	v_exp_f32_e32 v105, v105
	v_fma_f32 v101, v101, -2.0, 1.0
	v_add_f32_e32 v101, 1.0, v101
	v_mul_f32_e32 v101, v102, v101
	v_add_f32_e32 v102, 1.0, v105
	v_rcp_f32_e32 v102, v102
	v_lshlrev_b32_e32 v100, 16, v211
	v_add_f32_e32 v100, v103, v100
	v_mul_f32_e32 v100, v101, v100
	v_fma_f32 v102, v102, -2.0, 1.0
	v_and_b32_e32 v101, 0xffff0000, v211
	v_mul_f32_e32 v104, 0.5, v104
	v_add_f32_e32 v102, 1.0, v102
	v_add_f32_e32 v101, v106, v101
	v_mul_f32_e32 v102, v104, v102
	v_mul_f32_e32 v101, v102, v101
	v_cvt_pk_bf16_f32 v102, v100, v101
	ds_read_b64 v[100:101], v116 offset:2560
	ds_write_b32 v190, v102 offset:2688
	s_waitcnt lgkmcnt(1)
	v_lshlrev_b32_e32 v104, 16, v100
	v_mul_f32_e32 v104, 0x3fb8aa3b, v104
	v_exp_f32_e32 v104, v104
	v_and_b32_e32 v102, 0xffff0000, v100
	v_lshlrev_b32_e32 v100, 16, v101
	v_mul_f32_e32 v100, 0x3fb8aa3b, v100
	v_fmac_f32_e32 v102, v103, v104
	v_lshlrev_b32_e32 v103, 16, v217
	v_mul_f32_e32 v104, 0x3d372713, v103
	v_mul_f32_e32 v104, v104, v103
	v_fma_f32 v104, v104, v103, v103
	v_mul_f32_e32 v104, 0x3f4c422a, v104
	v_add_f32_e32 v104, v104, v104
	v_mul_f32_e32 v104, 0x3fb8aa3b, v104
	v_exp_f32_e32 v104, v104
	v_exp_f32_e32 v100, v100
	v_and_b32_e32 v105, 0xffff0000, v101
	v_mul_f32_e32 v103, 0.5, v103
	v_add_f32_e32 v101, 1.0, v104
	v_and_b32_e32 v104, 0xffff0000, v217
	v_fmac_f32_e32 v105, v106, v100
	v_mul_f32_e32 v106, 0x3d372713, v104
	v_mul_f32_e32 v106, v106, v104
	v_fma_f32 v106, v106, v104, v104
	v_mul_f32_e32 v106, 0x3f4c422a, v106
	v_rcp_f32_e32 v101, v101
	v_add_f32_e32 v106, v106, v106
	v_mul_f32_e32 v106, 0x3fb8aa3b, v106
	v_exp_f32_e32 v106, v106
	v_fma_f32 v101, v101, -2.0, 1.0
	v_add_f32_e32 v101, 1.0, v101
	v_mul_f32_e32 v101, v103, v101
	v_add_f32_e32 v103, 1.0, v106
	v_rcp_f32_e32 v103, v103
	v_lshlrev_b32_e32 v100, 16, v209
	v_add_f32_e32 v100, v102, v100
	v_mul_f32_e32 v100, v101, v100
	v_fma_f32 v103, v103, -2.0, 1.0
	v_and_b32_e32 v101, 0xffff0000, v209
	v_mul_f32_e32 v104, 0.5, v104
	v_add_f32_e32 v103, 1.0, v103
	v_add_f32_e32 v101, v105, v101
	v_mul_f32_e32 v103, v104, v103
	v_mul_f32_e32 v101, v103, v101
	v_cvt_pk_bf16_f32 v103, v100, v101
	ds_read_b64 v[100:101], v116 offset:2432
	ds_write_b32 v190, v103 offset:2560
	s_waitcnt lgkmcnt(1)
	v_lshlrev_b32_e32 v104, 16, v100
	v_mul_f32_e32 v104, 0x3fb8aa3b, v104
	v_exp_f32_e32 v104, v104
	v_and_b32_e32 v103, 0xffff0000, v100
	v_lshlrev_b32_e32 v100, 16, v101
	v_mul_f32_e32 v100, 0x3fb8aa3b, v100
	v_fmac_f32_e32 v103, v102, v104
	v_lshlrev_b32_e32 v102, 16, v215
	v_mul_f32_e32 v104, 0x3d372713, v102
	v_mul_f32_e32 v104, v104, v102
	v_fma_f32 v104, v104, v102, v102
	v_mul_f32_e32 v104, 0x3f4c422a, v104
	v_add_f32_e32 v104, v104, v104
	v_mul_f32_e32 v104, 0x3fb8aa3b, v104
	v_exp_f32_e32 v104, v104
	v_exp_f32_e32 v100, v100
	v_and_b32_e32 v106, 0xffff0000, v101
	v_mul_f32_e32 v102, 0.5, v102
	v_add_f32_e32 v101, 1.0, v104
	v_and_b32_e32 v104, 0xffff0000, v215
	v_fmac_f32_e32 v106, v105, v100
	v_mul_f32_e32 v105, 0x3d372713, v104
	v_mul_f32_e32 v105, v105, v104
	v_fma_f32 v105, v105, v104, v104
	v_mul_f32_e32 v105, 0x3f4c422a, v105
	v_rcp_f32_e32 v101, v101
	v_add_f32_e32 v105, v105, v105
	v_mul_f32_e32 v105, 0x3fb8aa3b, v105
	v_exp_f32_e32 v105, v105
	v_fma_f32 v101, v101, -2.0, 1.0
	v_add_f32_e32 v101, 1.0, v101
	v_mul_f32_e32 v101, v102, v101
	v_add_f32_e32 v102, 1.0, v105
	v_rcp_f32_e32 v102, v102
	v_lshlrev_b32_e32 v100, 16, v207
	v_add_f32_e32 v100, v103, v100
	v_mul_f32_e32 v100, v101, v100
	v_fma_f32 v102, v102, -2.0, 1.0
	v_and_b32_e32 v101, 0xffff0000, v207
	v_mul_f32_e32 v104, 0.5, v104
	v_add_f32_e32 v102, 1.0, v102
	v_add_f32_e32 v101, v106, v101
	v_mul_f32_e32 v102, v104, v102
	v_mul_f32_e32 v101, v102, v101
	v_cvt_pk_bf16_f32 v102, v100, v101
	ds_read_b64 v[100:101], v116 offset:2304
	ds_write_b32 v190, v102 offset:2432
	s_waitcnt lgkmcnt(1)
	v_lshlrev_b32_e32 v104, 16, v100
	v_mul_f32_e32 v104, 0x3fb8aa3b, v104
	v_exp_f32_e32 v104, v104
	v_and_b32_e32 v102, 0xffff0000, v100
	v_lshlrev_b32_e32 v100, 16, v101
	v_mul_f32_e32 v100, 0x3fb8aa3b, v100
	v_fmac_f32_e32 v102, v103, v104
	v_lshlrev_b32_e32 v103, 16, v213
	v_mul_f32_e32 v104, 0x3d372713, v103
	v_mul_f32_e32 v104, v104, v103
	v_fma_f32 v104, v104, v103, v103
	v_mul_f32_e32 v104, 0x3f4c422a, v104
	v_add_f32_e32 v104, v104, v104
	v_mul_f32_e32 v104, 0x3fb8aa3b, v104
	v_exp_f32_e32 v104, v104
	v_exp_f32_e32 v100, v100
	v_and_b32_e32 v105, 0xffff0000, v101
	v_mul_f32_e32 v103, 0.5, v103
	v_add_f32_e32 v101, 1.0, v104
	v_and_b32_e32 v104, 0xffff0000, v213
	v_fmac_f32_e32 v105, v106, v100
	v_mul_f32_e32 v106, 0x3d372713, v104
	v_mul_f32_e32 v106, v106, v104
	v_fma_f32 v106, v106, v104, v104
	v_mul_f32_e32 v106, 0x3f4c422a, v106
	v_rcp_f32_e32 v101, v101
	v_add_f32_e32 v106, v106, v106
	v_mul_f32_e32 v106, 0x3fb8aa3b, v106
	v_exp_f32_e32 v106, v106
	v_fma_f32 v101, v101, -2.0, 1.0
	v_add_f32_e32 v101, 1.0, v101
	v_mul_f32_e32 v101, v103, v101
	v_add_f32_e32 v103, 1.0, v106
	v_rcp_f32_e32 v103, v103
	v_lshlrev_b32_e32 v100, 16, v205
	v_add_f32_e32 v100, v102, v100
	v_mul_f32_e32 v100, v101, v100
	v_fma_f32 v103, v103, -2.0, 1.0
	v_and_b32_e32 v101, 0xffff0000, v205
	v_mul_f32_e32 v104, 0.5, v104
	v_add_f32_e32 v103, 1.0, v103
	v_add_f32_e32 v101, v105, v101
	v_mul_f32_e32 v103, v104, v103
	v_mul_f32_e32 v101, v103, v101
	v_cvt_pk_bf16_f32 v103, v100, v101
	ds_read_b64 v[100:101], v116 offset:2176
	ds_write_b32 v190, v103 offset:2304
	s_waitcnt lgkmcnt(1)
	v_lshlrev_b32_e32 v104, 16, v100
	v_mul_f32_e32 v104, 0x3fb8aa3b, v104
	v_exp_f32_e32 v104, v104
	v_and_b32_e32 v103, 0xffff0000, v100
	v_lshlrev_b32_e32 v100, 16, v101
	v_mul_f32_e32 v100, 0x3fb8aa3b, v100
	v_fmac_f32_e32 v103, v102, v104
	v_lshlrev_b32_e32 v102, 16, v212
	v_mul_f32_e32 v104, 0x3d372713, v102
	v_mul_f32_e32 v104, v104, v102
	v_fma_f32 v104, v104, v102, v102
	v_mul_f32_e32 v104, 0x3f4c422a, v104
	v_add_f32_e32 v104, v104, v104
	v_mul_f32_e32 v104, 0x3fb8aa3b, v104
	v_exp_f32_e32 v104, v104
	v_exp_f32_e32 v100, v100
	v_and_b32_e32 v106, 0xffff0000, v101
	v_mul_f32_e32 v102, 0.5, v102
	v_add_f32_e32 v101, 1.0, v104
	v_and_b32_e32 v104, 0xffff0000, v212
	v_fmac_f32_e32 v106, v105, v100
	v_mul_f32_e32 v105, 0x3d372713, v104
	v_mul_f32_e32 v105, v105, v104
	v_fma_f32 v105, v105, v104, v104
	v_mul_f32_e32 v105, 0x3f4c422a, v105
	v_rcp_f32_e32 v101, v101
	v_add_f32_e32 v105, v105, v105
	v_mul_f32_e32 v105, 0x3fb8aa3b, v105
	v_exp_f32_e32 v105, v105
	v_fma_f32 v101, v101, -2.0, 1.0
	v_add_f32_e32 v101, 1.0, v101
	v_mul_f32_e32 v101, v102, v101
	v_add_f32_e32 v102, 1.0, v105
	v_rcp_f32_e32 v102, v102
	v_lshlrev_b32_e32 v100, 16, v203
	v_add_f32_e32 v100, v103, v100
	v_mul_f32_e32 v100, v101, v100
	v_fma_f32 v102, v102, -2.0, 1.0
	v_and_b32_e32 v101, 0xffff0000, v203
	v_mul_f32_e32 v104, 0.5, v104
	v_add_f32_e32 v102, 1.0, v102
	v_add_f32_e32 v101, v106, v101
	v_mul_f32_e32 v102, v104, v102
	v_mul_f32_e32 v101, v102, v101
	v_cvt_pk_bf16_f32 v102, v100, v101
	ds_read_b64 v[100:101], v116 offset:2048
	ds_write_b32 v190, v102 offset:2176
	s_waitcnt lgkmcnt(1)
	v_lshlrev_b32_e32 v104, 16, v100
	v_mul_f32_e32 v104, 0x3fb8aa3b, v104
	v_exp_f32_e32 v104, v104
	v_and_b32_e32 v102, 0xffff0000, v100
	v_lshlrev_b32_e32 v100, 16, v101
	v_mul_f32_e32 v100, 0x3fb8aa3b, v100
	v_fmac_f32_e32 v102, v103, v104
	v_lshlrev_b32_e32 v103, 16, v210
	v_mul_f32_e32 v104, 0x3d372713, v103
	v_mul_f32_e32 v104, v104, v103
	v_fma_f32 v104, v104, v103, v103
	v_mul_f32_e32 v104, 0x3f4c422a, v104
	v_add_f32_e32 v104, v104, v104
	v_mul_f32_e32 v104, 0x3fb8aa3b, v104
	v_exp_f32_e32 v104, v104
	v_exp_f32_e32 v100, v100
	v_and_b32_e32 v105, 0xffff0000, v101
	v_mul_f32_e32 v103, 0.5, v103
	v_add_f32_e32 v101, 1.0, v104
	v_and_b32_e32 v104, 0xffff0000, v210
	v_fmac_f32_e32 v105, v106, v100
	v_mul_f32_e32 v106, 0x3d372713, v104
	v_mul_f32_e32 v106, v106, v104
	v_fma_f32 v106, v106, v104, v104
	v_mul_f32_e32 v106, 0x3f4c422a, v106
	v_rcp_f32_e32 v101, v101
	v_add_f32_e32 v106, v106, v106
	v_mul_f32_e32 v106, 0x3fb8aa3b, v106
	v_exp_f32_e32 v106, v106
	v_fma_f32 v101, v101, -2.0, 1.0
	v_add_f32_e32 v101, 1.0, v101
	v_mul_f32_e32 v101, v103, v101
	v_add_f32_e32 v103, 1.0, v106
	v_rcp_f32_e32 v103, v103
	v_lshlrev_b32_e32 v100, 16, v201
	v_add_f32_e32 v100, v102, v100
	v_mul_f32_e32 v100, v101, v100
	v_fma_f32 v103, v103, -2.0, 1.0
	v_and_b32_e32 v101, 0xffff0000, v201
	v_mul_f32_e32 v104, 0.5, v104
	v_add_f32_e32 v103, 1.0, v103
	v_add_f32_e32 v101, v105, v101
	v_mul_f32_e32 v103, v104, v103
	v_mul_f32_e32 v101, v103, v101
	v_cvt_pk_bf16_f32 v103, v100, v101
	ds_read_b64 v[100:101], v116 offset:1920
	ds_write_b32 v190, v103 offset:2048
	s_waitcnt lgkmcnt(1)
	v_lshlrev_b32_e32 v104, 16, v100
	v_mul_f32_e32 v104, 0x3fb8aa3b, v104
	v_exp_f32_e32 v104, v104
	v_and_b32_e32 v103, 0xffff0000, v100
	v_lshlrev_b32_e32 v100, 16, v101
	v_mul_f32_e32 v100, 0x3fb8aa3b, v100
	v_fmac_f32_e32 v103, v102, v104
	v_lshlrev_b32_e32 v102, 16, v208
	v_mul_f32_e32 v104, 0x3d372713, v102
	v_mul_f32_e32 v104, v104, v102
	v_fma_f32 v104, v104, v102, v102
	v_mul_f32_e32 v104, 0x3f4c422a, v104
	v_add_f32_e32 v104, v104, v104
	v_mul_f32_e32 v104, 0x3fb8aa3b, v104
	v_exp_f32_e32 v104, v104
	v_exp_f32_e32 v100, v100
	v_and_b32_e32 v106, 0xffff0000, v101
	v_mul_f32_e32 v102, 0.5, v102
	v_add_f32_e32 v101, 1.0, v104
	v_and_b32_e32 v104, 0xffff0000, v208
	v_fmac_f32_e32 v106, v105, v100
	v_mul_f32_e32 v105, 0x3d372713, v104
	v_mul_f32_e32 v105, v105, v104
	v_fma_f32 v105, v105, v104, v104
	v_mul_f32_e32 v105, 0x3f4c422a, v105
	v_rcp_f32_e32 v101, v101
	v_add_f32_e32 v105, v105, v105
	v_mul_f32_e32 v105, 0x3fb8aa3b, v105
	v_exp_f32_e32 v105, v105
	v_fma_f32 v101, v101, -2.0, 1.0
	v_add_f32_e32 v101, 1.0, v101
	v_mul_f32_e32 v101, v102, v101
	v_add_f32_e32 v102, 1.0, v105
	v_rcp_f32_e32 v102, v102
	v_lshlrev_b32_e32 v100, 16, v198
	v_add_f32_e32 v100, v103, v100
	v_mul_f32_e32 v100, v101, v100
	v_fma_f32 v102, v102, -2.0, 1.0
	v_and_b32_e32 v101, 0xffff0000, v198
	v_mul_f32_e32 v104, 0.5, v104
	v_add_f32_e32 v102, 1.0, v102
	v_add_f32_e32 v101, v106, v101
	v_mul_f32_e32 v102, v104, v102
	v_mul_f32_e32 v101, v102, v101
	v_cvt_pk_bf16_f32 v102, v100, v101
	ds_read_b64 v[100:101], v116 offset:1792
	ds_write_b32 v190, v102 offset:1920
	s_waitcnt lgkmcnt(1)
	v_lshlrev_b32_e32 v104, 16, v100
	v_mul_f32_e32 v104, 0x3fb8aa3b, v104
	v_exp_f32_e32 v104, v104
	v_and_b32_e32 v102, 0xffff0000, v100
	v_lshlrev_b32_e32 v100, 16, v101
	v_mul_f32_e32 v100, 0x3fb8aa3b, v100
	v_fmac_f32_e32 v102, v103, v104
	v_lshlrev_b32_e32 v103, 16, v206
	v_mul_f32_e32 v104, 0x3d372713, v103
	v_mul_f32_e32 v104, v104, v103
	v_fma_f32 v104, v104, v103, v103
	v_mul_f32_e32 v104, 0x3f4c422a, v104
	v_add_f32_e32 v104, v104, v104
	v_mul_f32_e32 v104, 0x3fb8aa3b, v104
	v_exp_f32_e32 v104, v104
	v_exp_f32_e32 v100, v100
	v_and_b32_e32 v105, 0xffff0000, v101
	v_mul_f32_e32 v103, 0.5, v103
	v_add_f32_e32 v101, 1.0, v104
	v_and_b32_e32 v104, 0xffff0000, v206
	v_fmac_f32_e32 v105, v106, v100
	v_mul_f32_e32 v106, 0x3d372713, v104
	v_mul_f32_e32 v106, v106, v104
	v_fma_f32 v106, v106, v104, v104
	v_mul_f32_e32 v106, 0x3f4c422a, v106
	v_rcp_f32_e32 v101, v101
	v_add_f32_e32 v106, v106, v106
	v_mul_f32_e32 v106, 0x3fb8aa3b, v106
	v_exp_f32_e32 v106, v106
	v_fma_f32 v101, v101, -2.0, 1.0
	v_add_f32_e32 v101, 1.0, v101
	v_mul_f32_e32 v101, v103, v101
	v_add_f32_e32 v103, 1.0, v106
	v_rcp_f32_e32 v103, v103
	v_lshlrev_b32_e32 v100, 16, v196
	v_add_f32_e32 v100, v102, v100
	v_mul_f32_e32 v100, v101, v100
	v_fma_f32 v103, v103, -2.0, 1.0
	v_and_b32_e32 v101, 0xffff0000, v196
	v_mul_f32_e32 v104, 0.5, v104
	v_add_f32_e32 v103, 1.0, v103
	v_add_f32_e32 v101, v105, v101
	v_mul_f32_e32 v103, v104, v103
	v_mul_f32_e32 v101, v103, v101
	v_cvt_pk_bf16_f32 v103, v100, v101
	ds_read_b64 v[100:101], v116 offset:1664
	ds_write_b32 v190, v103 offset:1792
	s_waitcnt lgkmcnt(1)
	v_lshlrev_b32_e32 v104, 16, v100
	v_mul_f32_e32 v104, 0x3fb8aa3b, v104
	v_exp_f32_e32 v104, v104
	v_and_b32_e32 v103, 0xffff0000, v100
	v_lshlrev_b32_e32 v100, 16, v101
	v_mul_f32_e32 v100, 0x3fb8aa3b, v100
	v_fmac_f32_e32 v103, v102, v104
	v_lshlrev_b32_e32 v102, 16, v204
	v_mul_f32_e32 v104, 0x3d372713, v102
	v_mul_f32_e32 v104, v104, v102
	v_fma_f32 v104, v104, v102, v102
	v_mul_f32_e32 v104, 0x3f4c422a, v104
	v_add_f32_e32 v104, v104, v104
	v_mul_f32_e32 v104, 0x3fb8aa3b, v104
	v_exp_f32_e32 v104, v104
	v_exp_f32_e32 v100, v100
	v_and_b32_e32 v106, 0xffff0000, v101
	v_mul_f32_e32 v102, 0.5, v102
	v_add_f32_e32 v101, 1.0, v104
	v_and_b32_e32 v104, 0xffff0000, v204
	v_fmac_f32_e32 v106, v105, v100
	v_mul_f32_e32 v105, 0x3d372713, v104
	v_mul_f32_e32 v105, v105, v104
	v_fma_f32 v105, v105, v104, v104
	v_mul_f32_e32 v105, 0x3f4c422a, v105
	v_rcp_f32_e32 v101, v101
	v_add_f32_e32 v105, v105, v105
	v_mul_f32_e32 v105, 0x3fb8aa3b, v105
	v_exp_f32_e32 v105, v105
	v_fma_f32 v101, v101, -2.0, 1.0
	v_add_f32_e32 v101, 1.0, v101
	v_mul_f32_e32 v101, v102, v101
	v_add_f32_e32 v102, 1.0, v105
	v_rcp_f32_e32 v102, v102
	v_lshlrev_b32_e32 v100, 16, v194
	v_add_f32_e32 v100, v103, v100
	v_mul_f32_e32 v100, v101, v100
	v_fma_f32 v102, v102, -2.0, 1.0
	v_and_b32_e32 v101, 0xffff0000, v194
	v_mul_f32_e32 v104, 0.5, v104
	v_add_f32_e32 v102, 1.0, v102
	v_add_f32_e32 v101, v106, v101
	v_mul_f32_e32 v102, v104, v102
	v_mul_f32_e32 v101, v102, v101
	v_cvt_pk_bf16_f32 v102, v100, v101
	ds_read_b64 v[100:101], v116 offset:1536
	ds_write_b32 v190, v102 offset:1664
	s_waitcnt lgkmcnt(1)
	v_lshlrev_b32_e32 v104, 16, v100
	v_mul_f32_e32 v104, 0x3fb8aa3b, v104
	v_exp_f32_e32 v104, v104
	v_and_b32_e32 v102, 0xffff0000, v100
	v_lshlrev_b32_e32 v100, 16, v101
	v_mul_f32_e32 v100, 0x3fb8aa3b, v100
	v_fmac_f32_e32 v102, v103, v104
	v_lshlrev_b32_e32 v103, 16, v202
	v_mul_f32_e32 v104, 0x3d372713, v103
	v_mul_f32_e32 v104, v104, v103
	v_fma_f32 v104, v104, v103, v103
	v_mul_f32_e32 v104, 0x3f4c422a, v104
	v_add_f32_e32 v104, v104, v104
	v_mul_f32_e32 v104, 0x3fb8aa3b, v104
	v_exp_f32_e32 v104, v104
	v_exp_f32_e32 v100, v100
	v_and_b32_e32 v105, 0xffff0000, v101
	v_mul_f32_e32 v103, 0.5, v103
	v_add_f32_e32 v101, 1.0, v104
	v_and_b32_e32 v104, 0xffff0000, v202
	v_fmac_f32_e32 v105, v106, v100
	v_mul_f32_e32 v106, 0x3d372713, v104
	v_mul_f32_e32 v106, v106, v104
	v_fma_f32 v106, v106, v104, v104
	v_mul_f32_e32 v106, 0x3f4c422a, v106
	v_rcp_f32_e32 v101, v101
	v_add_f32_e32 v106, v106, v106
	v_mul_f32_e32 v106, 0x3fb8aa3b, v106
	v_exp_f32_e32 v106, v106
	v_fma_f32 v101, v101, -2.0, 1.0
	v_add_f32_e32 v101, 1.0, v101
	v_mul_f32_e32 v101, v103, v101
	v_add_f32_e32 v103, 1.0, v106
	v_rcp_f32_e32 v103, v103
	v_lshlrev_b32_e32 v100, 16, v157
	v_add_f32_e32 v100, v102, v100
	v_mul_f32_e32 v100, v101, v100
	v_fma_f32 v103, v103, -2.0, 1.0
	v_and_b32_e32 v101, 0xffff0000, v157
	v_mul_f32_e32 v104, 0.5, v104
	v_add_f32_e32 v103, 1.0, v103
	v_add_f32_e32 v101, v105, v101
	v_mul_f32_e32 v103, v104, v103
	v_mul_f32_e32 v101, v103, v101
	v_cvt_pk_bf16_f32 v103, v100, v101
	ds_read_b64 v[100:101], v116 offset:1408
	ds_write_b32 v190, v103 offset:1536
	s_waitcnt lgkmcnt(1)
	v_lshlrev_b32_e32 v104, 16, v100
	v_mul_f32_e32 v104, 0x3fb8aa3b, v104
	v_exp_f32_e32 v104, v104
	v_and_b32_e32 v103, 0xffff0000, v100
	v_lshlrev_b32_e32 v100, 16, v101
	v_mul_f32_e32 v100, 0x3fb8aa3b, v100
	v_fmac_f32_e32 v103, v102, v104
	v_lshlrev_b32_e32 v102, 16, v200
	v_mul_f32_e32 v104, 0x3d372713, v102
	v_mul_f32_e32 v104, v104, v102
	v_fma_f32 v104, v104, v102, v102
	v_mul_f32_e32 v104, 0x3f4c422a, v104
	v_add_f32_e32 v104, v104, v104
	v_mul_f32_e32 v104, 0x3fb8aa3b, v104
	v_exp_f32_e32 v104, v104
	v_exp_f32_e32 v100, v100
	v_and_b32_e32 v106, 0xffff0000, v101
	v_mul_f32_e32 v102, 0.5, v102
	v_add_f32_e32 v101, 1.0, v104
	v_and_b32_e32 v104, 0xffff0000, v200
	v_fmac_f32_e32 v106, v105, v100
	v_mul_f32_e32 v105, 0x3d372713, v104
	v_mul_f32_e32 v105, v105, v104
	v_fma_f32 v105, v105, v104, v104
	v_mul_f32_e32 v105, 0x3f4c422a, v105
	v_rcp_f32_e32 v101, v101
	v_add_f32_e32 v105, v105, v105
	v_mul_f32_e32 v105, 0x3fb8aa3b, v105
	v_exp_f32_e32 v105, v105
	v_fma_f32 v101, v101, -2.0, 1.0
	v_add_f32_e32 v101, 1.0, v101
	v_mul_f32_e32 v101, v102, v101
	v_add_f32_e32 v102, 1.0, v105
	v_rcp_f32_e32 v102, v102
	v_lshlrev_b32_e32 v100, 16, v155
	v_add_f32_e32 v100, v103, v100
	v_mul_f32_e32 v100, v101, v100
	v_fma_f32 v102, v102, -2.0, 1.0
	v_and_b32_e32 v101, 0xffff0000, v155
	v_mul_f32_e32 v104, 0.5, v104
	v_add_f32_e32 v102, 1.0, v102
	v_add_f32_e32 v101, v106, v101
	v_mul_f32_e32 v102, v104, v102
	v_mul_f32_e32 v101, v102, v101
	v_cvt_pk_bf16_f32 v102, v100, v101
	ds_read_b64 v[100:101], v116 offset:1280
	ds_write_b32 v190, v102 offset:1408
	s_waitcnt lgkmcnt(1)
	v_lshlrev_b32_e32 v104, 16, v100
	v_mul_f32_e32 v104, 0x3fb8aa3b, v104
	v_exp_f32_e32 v104, v104
	v_and_b32_e32 v102, 0xffff0000, v100
	v_lshlrev_b32_e32 v100, 16, v101
	v_mul_f32_e32 v100, 0x3fb8aa3b, v100
	v_fmac_f32_e32 v102, v103, v104
	v_lshlrev_b32_e32 v103, 16, v199
	v_mul_f32_e32 v104, 0x3d372713, v103
	v_mul_f32_e32 v104, v104, v103
	v_fma_f32 v104, v104, v103, v103
	v_mul_f32_e32 v104, 0x3f4c422a, v104
	v_add_f32_e32 v104, v104, v104
	v_mul_f32_e32 v104, 0x3fb8aa3b, v104
	v_exp_f32_e32 v104, v104
	v_exp_f32_e32 v100, v100
	v_and_b32_e32 v105, 0xffff0000, v101
	v_mul_f32_e32 v103, 0.5, v103
	v_add_f32_e32 v101, 1.0, v104
	v_and_b32_e32 v104, 0xffff0000, v199
	v_fmac_f32_e32 v105, v106, v100
	v_mul_f32_e32 v106, 0x3d372713, v104
	v_mul_f32_e32 v106, v106, v104
	v_fma_f32 v106, v106, v104, v104
	v_mul_f32_e32 v106, 0x3f4c422a, v106
	v_rcp_f32_e32 v101, v101
	v_add_f32_e32 v106, v106, v106
	v_mul_f32_e32 v106, 0x3fb8aa3b, v106
	v_exp_f32_e32 v106, v106
	v_fma_f32 v101, v101, -2.0, 1.0
	v_add_f32_e32 v101, 1.0, v101
	v_mul_f32_e32 v101, v103, v101
	v_add_f32_e32 v103, 1.0, v106
	v_rcp_f32_e32 v103, v103
	v_lshlrev_b32_e32 v100, 16, v152
	v_add_f32_e32 v100, v102, v100
	v_mul_f32_e32 v100, v101, v100
	v_fma_f32 v103, v103, -2.0, 1.0
	v_and_b32_e32 v101, 0xffff0000, v152
	v_mul_f32_e32 v104, 0.5, v104
	v_add_f32_e32 v103, 1.0, v103
	v_add_f32_e32 v101, v105, v101
	v_mul_f32_e32 v103, v104, v103
	v_mul_f32_e32 v101, v103, v101
	v_cvt_pk_bf16_f32 v103, v100, v101
	ds_read_b64 v[100:101], v116 offset:1152
	ds_write_b32 v190, v103 offset:1280
	s_waitcnt lgkmcnt(1)
	v_lshlrev_b32_e32 v104, 16, v100
	v_mul_f32_e32 v104, 0x3fb8aa3b, v104
	v_exp_f32_e32 v104, v104
	v_and_b32_e32 v103, 0xffff0000, v100
	v_lshlrev_b32_e32 v100, 16, v101
	v_mul_f32_e32 v100, 0x3fb8aa3b, v100
	v_fmac_f32_e32 v103, v102, v104
	v_lshlrev_b32_e32 v102, 16, v197
	v_mul_f32_e32 v104, 0x3d372713, v102
	v_mul_f32_e32 v104, v104, v102
	v_fma_f32 v104, v104, v102, v102
	v_mul_f32_e32 v104, 0x3f4c422a, v104
	v_add_f32_e32 v104, v104, v104
	v_mul_f32_e32 v104, 0x3fb8aa3b, v104
	v_exp_f32_e32 v104, v104
	v_exp_f32_e32 v100, v100
	v_and_b32_e32 v106, 0xffff0000, v101
	v_mul_f32_e32 v102, 0.5, v102
	v_add_f32_e32 v101, 1.0, v104
	v_and_b32_e32 v104, 0xffff0000, v197
	v_fmac_f32_e32 v106, v105, v100
	v_mul_f32_e32 v105, 0x3d372713, v104
	v_mul_f32_e32 v105, v105, v104
	v_fma_f32 v105, v105, v104, v104
	v_mul_f32_e32 v105, 0x3f4c422a, v105
	v_rcp_f32_e32 v101, v101
	v_add_f32_e32 v105, v105, v105
	v_mul_f32_e32 v105, 0x3fb8aa3b, v105
	v_exp_f32_e32 v105, v105
	v_fma_f32 v101, v101, -2.0, 1.0
	v_add_f32_e32 v101, 1.0, v101
	v_mul_f32_e32 v101, v102, v101
	v_add_f32_e32 v102, 1.0, v105
	v_rcp_f32_e32 v102, v102
	v_lshlrev_b32_e32 v100, 16, v150
	v_add_f32_e32 v100, v103, v100
	v_mul_f32_e32 v100, v101, v100
	v_fma_f32 v102, v102, -2.0, 1.0
	v_and_b32_e32 v101, 0xffff0000, v150
	v_mul_f32_e32 v104, 0.5, v104
	v_add_f32_e32 v102, 1.0, v102
	v_add_f32_e32 v101, v106, v101
	v_mul_f32_e32 v102, v104, v102
	v_mul_f32_e32 v101, v102, v101
	v_cvt_pk_bf16_f32 v102, v100, v101
	ds_read_b64 v[100:101], v116 offset:1024
	ds_write_b32 v190, v102 offset:1152
	s_waitcnt lgkmcnt(1)
	v_lshlrev_b32_e32 v104, 16, v100
	v_mul_f32_e32 v104, 0x3fb8aa3b, v104
	v_exp_f32_e32 v104, v104
	v_and_b32_e32 v102, 0xffff0000, v100
	v_lshlrev_b32_e32 v100, 16, v101
	v_mul_f32_e32 v100, 0x3fb8aa3b, v100
	v_fmac_f32_e32 v102, v103, v104
	v_lshlrev_b32_e32 v103, 16, v195
	v_mul_f32_e32 v104, 0x3d372713, v103
	v_mul_f32_e32 v104, v104, v103
	v_fma_f32 v104, v104, v103, v103
	v_mul_f32_e32 v104, 0x3f4c422a, v104
	v_add_f32_e32 v104, v104, v104
	v_mul_f32_e32 v104, 0x3fb8aa3b, v104
	v_exp_f32_e32 v104, v104
	v_exp_f32_e32 v100, v100
	v_and_b32_e32 v105, 0xffff0000, v101
	v_mul_f32_e32 v103, 0.5, v103
	v_add_f32_e32 v101, 1.0, v104
	v_and_b32_e32 v104, 0xffff0000, v195
	v_fmac_f32_e32 v105, v106, v100
	v_mul_f32_e32 v106, 0x3d372713, v104
	v_mul_f32_e32 v106, v106, v104
	v_fma_f32 v106, v106, v104, v104
	v_mul_f32_e32 v106, 0x3f4c422a, v106
	v_rcp_f32_e32 v101, v101
	v_add_f32_e32 v106, v106, v106
	v_mul_f32_e32 v106, 0x3fb8aa3b, v106
	v_exp_f32_e32 v106, v106
	v_fma_f32 v101, v101, -2.0, 1.0
	v_add_f32_e32 v101, 1.0, v101
	v_mul_f32_e32 v101, v103, v101
	v_add_f32_e32 v103, 1.0, v106
	v_rcp_f32_e32 v103, v103
	v_lshlrev_b32_e32 v100, 16, v148
	v_add_f32_e32 v100, v102, v100
	v_mul_f32_e32 v100, v101, v100
	v_fma_f32 v103, v103, -2.0, 1.0
	v_and_b32_e32 v101, 0xffff0000, v148
	v_mul_f32_e32 v104, 0.5, v104
	v_add_f32_e32 v103, 1.0, v103
	v_add_f32_e32 v101, v105, v101
	v_mul_f32_e32 v103, v104, v103
	v_mul_f32_e32 v101, v103, v101
	v_cvt_pk_bf16_f32 v103, v100, v101
	ds_read_b64 v[100:101], v116 offset:896
	ds_write_b32 v190, v103 offset:1024
	s_waitcnt lgkmcnt(1)
	v_lshlrev_b32_e32 v104, 16, v100
	v_mul_f32_e32 v104, 0x3fb8aa3b, v104
	v_exp_f32_e32 v104, v104
	v_and_b32_e32 v103, 0xffff0000, v100
	v_lshlrev_b32_e32 v100, 16, v101
	v_mul_f32_e32 v100, 0x3fb8aa3b, v100
	v_fmac_f32_e32 v103, v102, v104
	v_lshlrev_b32_e32 v102, 16, v193
	v_mul_f32_e32 v104, 0x3d372713, v102
	v_mul_f32_e32 v104, v104, v102
	v_fma_f32 v104, v104, v102, v102
	v_mul_f32_e32 v104, 0x3f4c422a, v104
	v_add_f32_e32 v104, v104, v104
	v_mul_f32_e32 v104, 0x3fb8aa3b, v104
	v_exp_f32_e32 v104, v104
	v_exp_f32_e32 v100, v100
	v_and_b32_e32 v106, 0xffff0000, v101
	v_mul_f32_e32 v102, 0.5, v102
	v_add_f32_e32 v101, 1.0, v104
	v_and_b32_e32 v104, 0xffff0000, v193
	v_fmac_f32_e32 v106, v105, v100
	v_mul_f32_e32 v105, 0x3d372713, v104
	v_mul_f32_e32 v105, v105, v104
	v_fma_f32 v105, v105, v104, v104
	v_mul_f32_e32 v105, 0x3f4c422a, v105
	v_rcp_f32_e32 v101, v101
	v_add_f32_e32 v105, v105, v105
	v_mul_f32_e32 v105, 0x3fb8aa3b, v105
	v_exp_f32_e32 v105, v105
	v_fma_f32 v101, v101, -2.0, 1.0
	v_add_f32_e32 v101, 1.0, v101
	v_mul_f32_e32 v101, v102, v101
	v_add_f32_e32 v102, 1.0, v105
	v_rcp_f32_e32 v102, v102
	v_lshlrev_b32_e32 v100, 16, v146
	v_add_f32_e32 v100, v103, v100
	v_mul_f32_e32 v100, v101, v100
	v_fma_f32 v102, v102, -2.0, 1.0
	v_and_b32_e32 v101, 0xffff0000, v146
	v_mul_f32_e32 v104, 0.5, v104
	v_add_f32_e32 v102, 1.0, v102
	v_add_f32_e32 v101, v106, v101
	v_mul_f32_e32 v102, v104, v102
	v_mul_f32_e32 v101, v102, v101
	v_cvt_pk_bf16_f32 v102, v100, v101
	ds_read_b64 v[100:101], v116 offset:768
	ds_write_b32 v190, v102 offset:896
	s_waitcnt lgkmcnt(1)
	v_lshlrev_b32_e32 v104, 16, v100
	v_mul_f32_e32 v104, 0x3fb8aa3b, v104
	v_exp_f32_e32 v104, v104
	v_and_b32_e32 v102, 0xffff0000, v100
	v_lshlrev_b32_e32 v100, 16, v101
	v_mul_f32_e32 v100, 0x3fb8aa3b, v100
	v_fmac_f32_e32 v102, v103, v104
	v_lshlrev_b32_e32 v103, 16, v156
	v_mul_f32_e32 v104, 0x3d372713, v103
	v_mul_f32_e32 v104, v104, v103
	v_fma_f32 v104, v104, v103, v103
	v_mul_f32_e32 v104, 0x3f4c422a, v104
	v_add_f32_e32 v104, v104, v104
	v_mul_f32_e32 v104, 0x3fb8aa3b, v104
	v_exp_f32_e32 v104, v104
	v_exp_f32_e32 v100, v100
	v_and_b32_e32 v105, 0xffff0000, v101
	v_mul_f32_e32 v103, 0.5, v103
	v_add_f32_e32 v101, 1.0, v104
	v_and_b32_e32 v104, 0xffff0000, v156
	v_fmac_f32_e32 v105, v106, v100
	v_mul_f32_e32 v106, 0x3d372713, v104
	v_mul_f32_e32 v106, v106, v104
	v_fma_f32 v106, v106, v104, v104
	v_mul_f32_e32 v106, 0x3f4c422a, v106
	v_rcp_f32_e32 v101, v101
	v_add_f32_e32 v106, v106, v106
	v_mul_f32_e32 v106, 0x3fb8aa3b, v106
	v_exp_f32_e32 v106, v106
	v_fma_f32 v101, v101, -2.0, 1.0
	v_add_f32_e32 v101, 1.0, v101
	v_mul_f32_e32 v101, v103, v101
	v_add_f32_e32 v103, 1.0, v106
	v_rcp_f32_e32 v103, v103
	v_lshlrev_b32_e32 v100, 16, v144
	v_add_f32_e32 v100, v102, v100
	v_mul_f32_e32 v100, v101, v100
	v_fma_f32 v103, v103, -2.0, 1.0
	v_and_b32_e32 v101, 0xffff0000, v144
	v_mul_f32_e32 v104, 0.5, v104
	v_add_f32_e32 v103, 1.0, v103
	v_add_f32_e32 v101, v105, v101
	v_mul_f32_e32 v103, v104, v103
	v_mul_f32_e32 v101, v103, v101
	v_cvt_pk_bf16_f32 v103, v100, v101
	ds_read_b64 v[100:101], v116 offset:640
	ds_write_b32 v190, v103 offset:768
	s_waitcnt lgkmcnt(1)
	v_lshlrev_b32_e32 v104, 16, v100
	v_mul_f32_e32 v104, 0x3fb8aa3b, v104
	v_exp_f32_e32 v104, v104
	v_and_b32_e32 v103, 0xffff0000, v100
	v_lshlrev_b32_e32 v100, 16, v101
	v_mul_f32_e32 v100, 0x3fb8aa3b, v100
	v_fmac_f32_e32 v103, v102, v104
	v_lshlrev_b32_e32 v102, 16, v154
	v_mul_f32_e32 v104, 0x3d372713, v102
	v_mul_f32_e32 v104, v104, v102
	v_fma_f32 v104, v104, v102, v102
	v_mul_f32_e32 v104, 0x3f4c422a, v104
	v_add_f32_e32 v104, v104, v104
	v_mul_f32_e32 v104, 0x3fb8aa3b, v104
	v_exp_f32_e32 v104, v104
	v_exp_f32_e32 v100, v100
	v_and_b32_e32 v106, 0xffff0000, v101
	v_mul_f32_e32 v102, 0.5, v102
	v_add_f32_e32 v101, 1.0, v104
	v_and_b32_e32 v104, 0xffff0000, v154
	v_fmac_f32_e32 v106, v105, v100
	v_mul_f32_e32 v105, 0x3d372713, v104
	v_mul_f32_e32 v105, v105, v104
	v_fma_f32 v105, v105, v104, v104
	v_mul_f32_e32 v105, 0x3f4c422a, v105
	v_rcp_f32_e32 v101, v101
	v_add_f32_e32 v105, v105, v105
	v_mul_f32_e32 v105, 0x3fb8aa3b, v105
	v_exp_f32_e32 v105, v105
	v_fma_f32 v101, v101, -2.0, 1.0
	v_add_f32_e32 v101, 1.0, v101
	v_mul_f32_e32 v101, v102, v101
	v_add_f32_e32 v102, 1.0, v105
	v_rcp_f32_e32 v102, v102
	v_lshlrev_b32_e32 v100, 16, v143
	v_add_f32_e32 v100, v103, v100
	v_mul_f32_e32 v100, v101, v100
	v_fma_f32 v102, v102, -2.0, 1.0
	v_and_b32_e32 v101, 0xffff0000, v143
	v_mul_f32_e32 v104, 0.5, v104
	v_add_f32_e32 v102, 1.0, v102
	v_add_f32_e32 v101, v106, v101
	v_mul_f32_e32 v102, v104, v102
	v_mul_f32_e32 v101, v102, v101
	v_cvt_pk_bf16_f32 v102, v100, v101
	ds_read_b64 v[100:101], v116 offset:512
	ds_write_b32 v190, v102 offset:640
	s_waitcnt lgkmcnt(1)
	v_lshlrev_b32_e32 v104, 16, v100
	v_mul_f32_e32 v104, 0x3fb8aa3b, v104
	v_exp_f32_e32 v104, v104
	v_and_b32_e32 v102, 0xffff0000, v100
	v_lshlrev_b32_e32 v100, 16, v101
	v_mul_f32_e32 v100, 0x3fb8aa3b, v100
	v_fmac_f32_e32 v102, v103, v104
	v_lshlrev_b32_e32 v103, 16, v153
	v_mul_f32_e32 v104, 0x3d372713, v103
	v_mul_f32_e32 v104, v104, v103
	v_fma_f32 v104, v104, v103, v103
	v_mul_f32_e32 v104, 0x3f4c422a, v104
	v_add_f32_e32 v104, v104, v104
	v_mul_f32_e32 v104, 0x3fb8aa3b, v104
	v_exp_f32_e32 v104, v104
	v_exp_f32_e32 v100, v100
	v_and_b32_e32 v105, 0xffff0000, v101
	v_mul_f32_e32 v103, 0.5, v103
	v_add_f32_e32 v101, 1.0, v104
	v_and_b32_e32 v104, 0xffff0000, v153
	v_fmac_f32_e32 v105, v106, v100
	v_mul_f32_e32 v106, 0x3d372713, v104
	v_mul_f32_e32 v106, v106, v104
	v_fma_f32 v106, v106, v104, v104
	v_mul_f32_e32 v106, 0x3f4c422a, v106
	v_rcp_f32_e32 v101, v101
	v_add_f32_e32 v106, v106, v106
	v_mul_f32_e32 v106, 0x3fb8aa3b, v106
	v_exp_f32_e32 v106, v106
	v_fma_f32 v101, v101, -2.0, 1.0
	v_add_f32_e32 v101, 1.0, v101
	v_mul_f32_e32 v101, v103, v101
	v_add_f32_e32 v103, 1.0, v106
	v_rcp_f32_e32 v103, v103
	v_lshlrev_b32_e32 v100, 16, v142
	v_add_f32_e32 v100, v102, v100
	v_mul_f32_e32 v100, v101, v100
	v_fma_f32 v103, v103, -2.0, 1.0
	v_and_b32_e32 v101, 0xffff0000, v142
	v_mul_f32_e32 v104, 0.5, v104
	v_add_f32_e32 v103, 1.0, v103
	v_add_f32_e32 v101, v105, v101
	v_mul_f32_e32 v103, v104, v103
	v_mul_f32_e32 v101, v103, v101
	v_cvt_pk_bf16_f32 v103, v100, v101
	ds_read_b64 v[100:101], v116 offset:384
	ds_write_b32 v190, v103 offset:512
	s_waitcnt lgkmcnt(1)
	v_lshlrev_b32_e32 v104, 16, v100
	v_mul_f32_e32 v104, 0x3fb8aa3b, v104
	v_exp_f32_e32 v104, v104
	v_and_b32_e32 v103, 0xffff0000, v100
	v_lshlrev_b32_e32 v100, 16, v101
	v_mul_f32_e32 v100, 0x3fb8aa3b, v100
	v_fmac_f32_e32 v103, v102, v104
	v_lshlrev_b32_e32 v102, 16, v151
	v_mul_f32_e32 v104, 0x3d372713, v102
	v_mul_f32_e32 v104, v104, v102
	v_fma_f32 v104, v104, v102, v102
	v_mul_f32_e32 v104, 0x3f4c422a, v104
	v_add_f32_e32 v104, v104, v104
	v_mul_f32_e32 v104, 0x3fb8aa3b, v104
	v_exp_f32_e32 v104, v104
	v_exp_f32_e32 v100, v100
	v_and_b32_e32 v106, 0xffff0000, v101
	v_mul_f32_e32 v102, 0.5, v102
	v_add_f32_e32 v101, 1.0, v104
	v_and_b32_e32 v104, 0xffff0000, v151
	v_fmac_f32_e32 v106, v105, v100
	v_mul_f32_e32 v105, 0x3d372713, v104
	v_mul_f32_e32 v105, v105, v104
	v_fma_f32 v105, v105, v104, v104
	v_mul_f32_e32 v105, 0x3f4c422a, v105
	v_rcp_f32_e32 v101, v101
	v_add_f32_e32 v105, v105, v105
	v_mul_f32_e32 v105, 0x3fb8aa3b, v105
	v_exp_f32_e32 v105, v105
	v_fma_f32 v101, v101, -2.0, 1.0
	v_add_f32_e32 v101, 1.0, v101
	v_mul_f32_e32 v101, v102, v101
	v_add_f32_e32 v102, 1.0, v105
	v_rcp_f32_e32 v102, v102
	v_lshlrev_b32_e32 v100, 16, v141
	v_add_f32_e32 v100, v103, v100
	v_mul_f32_e32 v100, v101, v100
	v_fma_f32 v102, v102, -2.0, 1.0
	v_and_b32_e32 v101, 0xffff0000, v141
	v_mul_f32_e32 v104, 0.5, v104
	v_add_f32_e32 v102, 1.0, v102
	v_add_f32_e32 v101, v106, v101
	v_mul_f32_e32 v102, v104, v102
	v_mul_f32_e32 v101, v102, v101
	v_cvt_pk_bf16_f32 v102, v100, v101
	ds_read_b64 v[100:101], v116 offset:256
	ds_write_b32 v190, v102 offset:384
	s_waitcnt lgkmcnt(1)
	v_lshlrev_b32_e32 v104, 16, v100
	v_mul_f32_e32 v104, 0x3fb8aa3b, v104
	v_exp_f32_e32 v104, v104
	v_and_b32_e32 v102, 0xffff0000, v100
	v_lshlrev_b32_e32 v100, 16, v101
	v_mul_f32_e32 v100, 0x3fb8aa3b, v100
	v_fmac_f32_e32 v102, v103, v104
	v_lshlrev_b32_e32 v103, 16, v149
	v_mul_f32_e32 v104, 0x3d372713, v103
	v_mul_f32_e32 v104, v104, v103
	v_fma_f32 v104, v104, v103, v103
	v_mul_f32_e32 v104, 0x3f4c422a, v104
	v_add_f32_e32 v104, v104, v104
	v_mul_f32_e32 v104, 0x3fb8aa3b, v104
	v_exp_f32_e32 v104, v104
	v_exp_f32_e32 v100, v100
	v_and_b32_e32 v105, 0xffff0000, v101
	v_mul_f32_e32 v103, 0.5, v103
	v_add_f32_e32 v101, 1.0, v104
	v_and_b32_e32 v104, 0xffff0000, v149
	v_fmac_f32_e32 v105, v106, v100
	v_mul_f32_e32 v106, 0x3d372713, v104
	v_mul_f32_e32 v106, v106, v104
	v_fma_f32 v106, v106, v104, v104
	v_mul_f32_e32 v106, 0x3f4c422a, v106
	v_rcp_f32_e32 v101, v101
	v_add_f32_e32 v106, v106, v106
	v_mul_f32_e32 v106, 0x3fb8aa3b, v106
	v_exp_f32_e32 v106, v106
	v_fma_f32 v101, v101, -2.0, 1.0
	v_add_f32_e32 v101, 1.0, v101
	v_mul_f32_e32 v101, v103, v101
	v_add_f32_e32 v103, 1.0, v106
	v_rcp_f32_e32 v103, v103
	v_lshlrev_b32_e32 v100, 16, v140
	v_add_f32_e32 v100, v102, v100
	v_mul_f32_e32 v100, v101, v100
	v_fma_f32 v103, v103, -2.0, 1.0
	v_and_b32_e32 v101, 0xffff0000, v140
	v_mul_f32_e32 v104, 0.5, v104
	v_add_f32_e32 v103, 1.0, v103
	v_add_f32_e32 v101, v105, v101
	v_mul_f32_e32 v103, v104, v103
	v_mul_f32_e32 v101, v103, v101
	v_cvt_pk_bf16_f32 v103, v100, v101
	ds_read_b64 v[100:101], v116 offset:128
	ds_write_b32 v190, v103 offset:256
	s_waitcnt lgkmcnt(1)
	v_lshlrev_b32_e32 v104, 16, v100
	v_mul_f32_e32 v104, 0x3fb8aa3b, v104
	v_exp_f32_e32 v104, v104
	v_and_b32_e32 v103, 0xffff0000, v100
	v_lshlrev_b32_e32 v100, 16, v101
	v_mul_f32_e32 v100, 0x3fb8aa3b, v100
	v_fmac_f32_e32 v103, v102, v104
	v_lshlrev_b32_e32 v102, 16, v147
	v_mul_f32_e32 v104, 0x3d372713, v102
	v_mul_f32_e32 v104, v104, v102
	v_fma_f32 v104, v104, v102, v102
	v_mul_f32_e32 v104, 0x3f4c422a, v104
	v_add_f32_e32 v104, v104, v104
	v_mul_f32_e32 v104, 0x3fb8aa3b, v104
	v_exp_f32_e32 v104, v104
	v_exp_f32_e32 v100, v100
	v_and_b32_e32 v106, 0xffff0000, v101
	v_mul_f32_e32 v102, 0.5, v102
	v_add_f32_e32 v101, 1.0, v104
	v_and_b32_e32 v104, 0xffff0000, v147
	v_fmac_f32_e32 v106, v105, v100
	v_mul_f32_e32 v105, 0x3d372713, v104
	v_mul_f32_e32 v105, v105, v104
	v_fma_f32 v105, v105, v104, v104
	v_mul_f32_e32 v105, 0x3f4c422a, v105
	v_rcp_f32_e32 v101, v101
	v_add_f32_e32 v105, v105, v105
	v_mul_f32_e32 v105, 0x3fb8aa3b, v105
	v_exp_f32_e32 v105, v105
	v_fma_f32 v101, v101, -2.0, 1.0
	v_add_f32_e32 v101, 1.0, v101
	v_mul_f32_e32 v101, v102, v101
	v_add_f32_e32 v102, 1.0, v105
	v_rcp_f32_e32 v102, v102
	v_lshlrev_b32_e32 v100, 16, v139
	v_add_f32_e32 v100, v103, v100
	v_mul_f32_e32 v100, v101, v100
	v_fma_f32 v102, v102, -2.0, 1.0
	v_and_b32_e32 v101, 0xffff0000, v139
	v_mul_f32_e32 v104, 0.5, v104
	v_add_f32_e32 v102, 1.0, v102
	v_add_f32_e32 v101, v106, v101
	v_mul_f32_e32 v102, v104, v102
	v_mul_f32_e32 v101, v102, v101
	v_cvt_pk_bf16_f32 v102, v100, v101
	ds_read_b64 v[100:101], v116
	ds_write_b32 v190, v102 offset:128
	s_waitcnt lgkmcnt(1)
	v_lshlrev_b32_e32 v104, 16, v100
	v_mul_f32_e32 v104, 0x3fb8aa3b, v104
	v_exp_f32_e32 v104, v104
	v_and_b32_e32 v100, 0xffff0000, v100
	v_lshlrev_b32_e32 v102, 16, v101
	v_mul_f32_e32 v102, 0x3fb8aa3b, v102
	v_fmac_f32_e32 v100, v103, v104
	v_lshlrev_b32_e32 v103, 16, v145
	v_mul_f32_e32 v104, 0x3d372713, v103
	v_mul_f32_e32 v104, v104, v103
	v_fma_f32 v104, v104, v103, v103
	v_mul_f32_e32 v104, 0x3f4c422a, v104
	v_add_f32_e32 v104, v104, v104
	v_mul_f32_e32 v104, 0x3fb8aa3b, v104
	v_exp_f32_e32 v104, v104
	v_exp_f32_e32 v102, v102
	v_and_b32_e32 v101, 0xffff0000, v101
	v_mul_f32_e32 v103, 0.5, v103
	v_add_f32_e32 v104, 1.0, v104
	v_rcp_f32_e32 v104, v104
	v_fmac_f32_e32 v101, v106, v102
	v_lshlrev_b32_e32 v102, 16, v138
	v_add_f32_e32 v100, v100, v102
	v_fma_f32 v102, v104, -2.0, 1.0
	v_and_b32_e32 v104, 0xffff0000, v145
	v_mul_f32_e32 v105, 0x3d372713, v104
	v_mul_f32_e32 v105, v105, v104
	v_fma_f32 v105, v105, v104, v104
	v_mul_f32_e32 v105, 0x3f4c422a, v105
	v_add_f32_e32 v105, v105, v105
	v_mul_f32_e32 v105, 0x3fb8aa3b, v105
	v_exp_f32_e32 v105, v105
	v_add_f32_e32 v102, 1.0, v102
	v_mul_f32_e32 v102, v103, v102
	v_mul_f32_e32 v100, v102, v100
	v_add_f32_e32 v103, 1.0, v105
	v_rcp_f32_e32 v103, v103
	v_and_b32_e32 v102, 0xffff0000, v138
	v_add_f32_e32 v101, v101, v102
	v_fma_f32 v102, v103, -2.0, 1.0
	v_mul_f32_e32 v103, 0.5, v104
	v_add_f32_e32 v102, 1.0, v102
	v_mul_f32_e32 v102, v103, v102
	v_mul_f32_e32 v101, v102, v101
	v_cvt_pk_bf16_f32 v100, v100, v101
	ds_write_b32 v190, v100
	v_or_b32_e32 v102, s44, v72
	v_mov_b64_e32 v[100:101], s[20:21]
	v_mad_u64_u32 v[100:101], s[48:49], v102, s52, v[100:101]
	v_mad_i32_i24 v101, s45, v192, v101
	v_lshl_add_u64 v[100:101], s[42:43], 1, v[100:101]
	v_lshl_add_u64 v[100:101], v[100:101], 0, s[36:37]
	v_lshl_add_u64 v[104:105], v[100:101], 0, v[70:71]
	ds_read_b128 v[100:103], v191
	s_waitcnt lgkmcnt(0)
	global_store_dwordx4 v[104:105], v[100:103], off
	v_lshl_add_u64 v[104:105], v[104:105], 0, s[40:41]
	ds_read_b128 v[100:103], v191 offset:2048
	s_waitcnt lgkmcnt(0)
	global_store_dwordx4 v[104:105], v[100:103], off
	v_lshl_add_u64 v[104:105], v[104:105], 0, s[40:41]
	ds_read_b128 v[100:103], v191 offset:4224
	s_waitcnt lgkmcnt(0)
	global_store_dwordx4 v[104:105], v[100:103], off
	v_lshl_add_u64 v[104:105], v[104:105], 0, s[40:41]
	ds_read_b128 v[100:103], v191 offset:6272
	s_waitcnt lgkmcnt(0)
	global_store_dwordx4 v[104:105], v[100:103], off
	v_lshl_add_u64 v[104:105], v[104:105], 0, s[40:41]
	ds_read_b128 v[100:103], v191 offset:8448
	s_waitcnt lgkmcnt(0)
	global_store_dwordx4 v[104:105], v[100:103], off
	v_lshl_add_u64 v[104:105], v[104:105], 0, s[40:41]
	ds_read_b128 v[100:103], v191 offset:10496
	s_waitcnt lgkmcnt(0)
	global_store_dwordx4 v[104:105], v[100:103], off
	v_lshl_add_u64 v[104:105], v[104:105], 0, s[40:41]
	ds_read_b128 v[100:103], v191 offset:12672
	s_waitcnt lgkmcnt(0)
	global_store_dwordx4 v[104:105], v[100:103], off
	v_lshl_add_u64 v[104:105], v[104:105], 0, s[40:41]
	ds_read_b128 v[100:103], v191 offset:14720
	s_waitcnt lgkmcnt(0)
	global_store_dwordx4 v[104:105], v[100:103], off
	s_cbranch_vccz .LBB0_1505
